# baseline (speedup 1.0000x reference)
.LE_loop12:
	s_sub_u32 s71, s33, 1
	s_add_u32 s61, s33, 1
	s_min_u32 s61, s61, s60
	s_and_b32 s64, s71, 1
	s_lshl_b32 s64, s64, 22
	s_add_u32 s64, s64, s50
	s_add_u32 s64, s64, 0x60000
	s_add_u32 s36, s6, s64
	s_addc_u32 s37, s7, 0
	s_lshl_b32 s64, s71, 3
	s_add_u32 s64, s64, s29
	s_lshl_b32 s64, s64, 5
	s_add_u32 s64, s64, s30
	s_lshl_b32 s64, s64, 2
	s_add_u32 s40, s8, s64
	s_addc_u32 s41, s9, 0
	s_lshl_b32 s64, s33, 11
	s_lshl_b32 s65, s29, 8
	s_add_u32 s64, s64, s65
	s_add_u32 s64, s64, 128
	s_lshl_b32 s64, s64, 3
	s_add_u32 s42, s12, s64
	s_addc_u32 s43, s13, 0
	s_nop 3
	global_load_dword v228, v249, s[42:43] offset:0
	global_load_dword v229, v249, s[42:43] offset:256
	s_waitcnt lgkmcnt(2)
	v_mfma_f32_32x32x16_f16 v[0:15], a[0:3], v[160:163], v[0:15]
	ds_read_b128 v[160:163], v192 offset:8192
	v_exp_f32_e32 v200, v96
	v_mfma_f32_32x32x16_f16 v[16:31], a[0:3], v[164:167], v[16:31]
	ds_read_b128 v[164:167], v192 offset:9216
	s_lshl_b32 s64, s71, 3
	s_add_u32 s64, s64, s29
	s_lshl_b32 s64, s64, 7
	s_add_u32 s38, s8, s64
	s_addc_u32 s39, s9, 0
	global_load_dword v251, v196, s[38:39] sc1
	v_exp_f32_e32 v201, v97
	v_add_f32_e32 v200, 1.0, v200
	v_mfma_f32_32x32x16_f16 v[0:15], a[4:7], v[168:171], v[0:15]
	ds_read_b128 v[168:171], v192 offset:10240
	v_exp_f32_e32 v202, v98
	v_add_f32_e32 v201, 1.0, v201
	v_mfma_f32_32x32x16_f16 v[16:31], a[4:7], v[172:175], v[16:31]
	ds_read_b128 v[172:175], v192 offset:11264
	global_load_lds_dwordx4 v192, s[44:45] offset:1024 sc1
	v_exp_f32_e32 v203, v99
	v_add_f32_e32 v202, 1.0, v202
	v_mfma_f32_32x32x16_f16 v[0:15], a[8:11], v[176:179], v[0:15]
	ds_read_b128 v[176:179], v192 offset:12288
	v_exp_f32_e32 v204, v100
	v_add_f32_e32 v203, 1.0, v203
	v_mfma_f32_32x32x16_f16 v[16:31], a[8:11], v[180:183], v[16:31]
	ds_read_b128 v[180:183], v192 offset:13312
	v_exp_f32_e32 v205, v101
	v_add_f32_e32 v204, 1.0, v204
	s_waitcnt lgkmcnt(2)
	v_mfma_f32_32x32x16_f16 v[0:15], a[12:15], v[184:187], v[0:15]
	ds_read_b128 v[184:187], v192 offset:14336
	v_exp_f32_e32 v206, v102
	v_add_f32_e32 v205, 1.0, v205
	v_mfma_f32_32x32x16_f16 v[16:31], a[12:15], v[188:191], v[16:31]
	ds_read_b128 v[188:191], v192 offset:15360
	global_load_lds_dwordx4 v192, s[44:45] offset:2048 sc1
	v_exp_f32_e32 v207, v103
	v_add_f32_e32 v206, 1.0, v206
	v_mfma_f32_32x32x16_f16 v[0:15], a[16:19], v[160:163], v[0:15]
	ds_read_b128 v[160:163], v192 offset:16384
	v_exp_f32_e32 v208, v104
	v_add_f32_e32 v207, 1.0, v207
	v_mfma_f32_32x32x16_f16 v[16:31], a[16:19], v[164:167], v[16:31]
	ds_read_b128 v[164:167], v192 offset:17408
	v_exp_f32_e32 v209, v105
	v_add_f32_e32 v208, 1.0, v208
	v_mfma_f32_32x32x16_f16 v[0:15], a[20:23], v[168:171], v[0:15]
	ds_read_b128 v[168:171], v192 offset:18432
	v_exp_f32_e32 v210, v106
	v_add_f32_e32 v209, 1.0, v209
	v_mfma_f32_32x32x16_f16 v[16:31], a[20:23], v[172:175], v[16:31]
	ds_read_b128 v[172:175], v192 offset:19456
	global_load_lds_dwordx4 v192, s[44:45] offset:3072 sc1
	v_exp_f32_e32 v211, v107
	v_add_f32_e32 v210, 1.0, v210
	s_waitcnt lgkmcnt(2)
	v_mfma_f32_32x32x16_f16 v[0:15], a[24:27], v[176:179], v[0:15]
	ds_read_b128 v[176:179], v192 offset:20480
	v_exp_f32_e32 v212, v108
	v_add_f32_e32 v211, 1.0, v211
	v_mfma_f32_32x32x16_f16 v[16:31], a[24:27], v[180:183], v[16:31]
	ds_read_b128 v[180:183], v192 offset:21504
	v_exp_f32_e32 v213, v109
	v_add_f32_e32 v212, 1.0, v212
	v_mfma_f32_32x32x16_f16 v[0:15], a[28:31], v[184:187], v[0:15]
	ds_read_b128 v[184:187], v192 offset:22528
	v_exp_f32_e32 v214, v110
	v_add_f32_e32 v213, 1.0, v213
	v_mfma_f32_32x32x16_f16 v[16:31], a[28:31], v[188:191], v[16:31]
	ds_read_b128 v[188:191], v192 offset:23552
	s_mov_b32 m0, s57
	s_add_u32 s44, s34, 0x11000
	s_addc_u32 s45, s35, 0
	global_load_lds_dwordx4 v192, s[44:45] sc1
	v_exp_f32_e32 v215, v111
	v_add_f32_e32 v214, 1.0, v214
	v_mfma_f32_32x32x16_f16 v[0:15], a[32:35], v[160:163], v[0:15]
	ds_read_b128 v[160:163], v192 offset:24576
	v_add_f32_e32 v215, 1.0, v215
	v_rcp_f32_e32 v200, v200
	v_mfma_f32_32x32x16_f16 v[16:31], a[32:35], v[164:167], v[16:31]
	ds_read_b128 v[164:167], v192 offset:25600
	v_rcp_f32_e32 v201, v201
	s_waitcnt lgkmcnt(2)
	v_mfma_f32_32x32x16_f16 v[0:15], a[36:39], v[168:171], v[0:15]
	ds_read_b128 v[168:171], v192 offset:26624
	v_rcp_f32_e32 v202, v202
	v_mfma_f32_32x32x16_f16 v[16:31], a[36:39], v[172:175], v[16:31]
	ds_read_b128 v[172:175], v192 offset:27648
	global_load_lds_dwordx4 v192, s[44:45] offset:1024 sc1
	v_rcp_f32_e32 v203, v203
	v_mfma_f32_32x32x16_f16 v[0:15], a[40:43], v[176:179], v[0:15]
	ds_read_b128 v[176:179], v192 offset:28672
	v_rcp_f32_e32 v204, v204
	v_mfma_f32_32x32x16_f16 v[16:31], a[40:43], v[180:183], v[16:31]
	ds_read_b128 v[180:183], v192 offset:29696
	v_rcp_f32_e32 v205, v205
	v_mul_f32_e32 v204, v204, v152
	v_mfma_f32_32x32x16_f16 v[0:15], a[44:47], v[184:187], v[0:15]
	ds_read_b128 v[184:187], v192 offset:30720
	v_rcp_f32_e32 v206, v206
	v_mul_f32_e32 v205, v205, v153
	v_mfma_f32_32x32x16_f16 v[16:31], a[44:47], v[188:191], v[16:31]
	ds_read_b128 v[188:191], v192 offset:31744
	global_load_lds_dwordx4 v192, s[44:45] offset:2048 sc1
	v_rcp_f32_e32 v207, v207
	v_mul_f32_e32 v206, v206, v154
	s_waitcnt vmcnt(10)
	s_barrier
	s_waitcnt lgkmcnt(2)
	v_mfma_f32_32x32x16_f16 v[0:15], a[48:51], v[160:163], v[0:15]
	ds_read_b128 v[160:163], v192 offset:32768
	v_rcp_f32_e32 v208, v208
	v_mul_f32_e32 v207, v207, v155
	v_mfma_f32_32x32x16_f16 v[16:31], a[48:51], v[164:167], v[16:31]
	ds_read_b128 v[164:167], v192 offset:33792
	v_rcp_f32_e32 v209, v209
	v_fmamk_f32 v208, v208, 0xc0b8aa3b, v198
	v_mfma_f32_32x32x16_f16 v[0:15], a[52:55], v[168:171], v[0:15]
	ds_read_b128 v[168:171], v192 offset:34816
	v_rcp_f32_e32 v210, v210
	v_fmamk_f32 v209, v209, 0xc0b8aa3b, v198
	v_fma_f32 v152, v200, v208, v204
	v_mfma_f32_32x32x16_f16 v[16:31], a[52:55], v[172:175], v[16:31]
	ds_read_b128 v[172:175], v192 offset:35840
	global_load_lds_dwordx4 v192, s[44:45] offset:3072 sc1
	v_rcp_f32_e32 v211, v211
	v_fmamk_f32 v210, v210, 0xc0b8aa3b, v198
	v_fma_f32 v153, v201, v209, v205
	v_mfma_f32_32x32x16_f16 v[0:15], a[56:59], v[176:179], v[0:15]
	ds_read_b128 v[176:179], v192 offset:36864
	v_rcp_f32_e32 v212, v212
	v_fmamk_f32 v211, v211, 0xc0b8aa3b, v198
	v_fma_f32 v154, v202, v210, v206
	v_mfma_f32_32x32x16_f16 v[16:31], a[56:59], v[180:183], v[16:31]
	ds_read_b128 v[180:183], v192 offset:37888
	v_rcp_f32_e32 v213, v213
	v_fma_f32 v155, v203, v211, v207
	s_waitcnt lgkmcnt(2)
	v_mfma_f32_32x32x16_f16 v[0:15], a[60:63], v[184:187], v[0:15]
	ds_read_b128 v[184:187], v192 offset:38912
	v_rcp_f32_e32 v214, v214
	v_mfma_f32_32x32x16_f16 v[16:31], a[60:63], v[188:191], v[16:31]
	ds_read_b128 v[188:191], v192 offset:39936
	s_mov_b32 m0, s58
	s_add_u32 s44, s34, 0x18000
	s_addc_u32 s45, s35, 0
	global_load_lds_dwordx4 v192, s[44:45] sc1
	v_rcp_f32_e32 v215, v215
	v_mfma_f32_32x32x16_f16 v[0:15], a[64:67], v[160:163], v[0:15]
	ds_read_b128 v[160:163], v192 offset:40960
	v_exp_f32_e32 v200, v152
	v_mfma_f32_32x32x16_f16 v[16:31], a[64:67], v[164:167], v[16:31]
	ds_read_b128 v[164:167], v192 offset:41984
	v_exp_f32_e32 v201, v153
	v_add_f32_e32 v200, 1.0, v200
	v_mfma_f32_32x32x16_f16 v[0:15], a[68:71], v[168:171], v[0:15]
	ds_read_b128 v[168:171], v192 offset:43008
	v_exp_f32_e32 v202, v154
	v_add_f32_e32 v201, 1.0, v201
	v_mfma_f32_32x32x16_f16 v[16:31], a[68:71], v[172:175], v[16:31]
	ds_read_b128 v[172:175], v192 offset:44032
	global_load_lds_dwordx4 v192, s[44:45] offset:1024 sc1
	v_exp_f32_e32 v203, v155
	v_add_f32_e32 v202, 1.0, v202
	s_waitcnt lgkmcnt(2)
	v_mfma_f32_32x32x16_f16 v[0:15], a[72:75], v[176:179], v[0:15]
	ds_read_b128 v[176:179], v192 offset:45056
	v_add_f32_e32 v203, 1.0, v203
	v_rcp_f32_e32 v200, v200
	v_mfma_f32_32x32x16_f16 v[16:31], a[72:75], v[180:183], v[16:31]
	ds_read_b128 v[180:183], v192 offset:46080
	v_rcp_f32_e32 v201, v201
	v_fma_f32 v200, v200, 2.0, -1.0
	v_mfma_f32_32x32x16_f16 v[0:15], a[76:79], v[184:187], v[0:15]
	ds_read_b128 v[184:187], v192 offset:47104
	v_rcp_f32_e32 v202, v202
	v_fma_f32 v201, v201, 2.0, -1.0
	v_mul_f32_e32 v216, v212, v200
	v_mfma_f32_32x32x16_f16 v[16:31], a[76:79], v[188:191], v[16:31]
	ds_read_b128 v[188:191], v192 offset:48128
	global_load_lds_dwordx4 v192, s[44:45] offset:2048 sc1
	v_rcp_f32_e32 v203, v203
	v_fma_f32 v202, v202, 2.0, -1.0
	v_mul_f32_e32 v217, v213, v201
	v_mfma_f32_32x32x16_f16 v[0:15], a[80:83], v[160:163], v[0:15]
	ds_read_b128 v[160:163], v192 offset:49152
	v_fma_f32 v203, v203, 2.0, -1.0
	v_mul_f32_e32 v218, v214, v202
	v_exp_f32_e32 v200, v112
	v_mfma_f32_32x32x16_f16 v[16:31], a[80:83], v[164:167], v[16:31]
	ds_read_b128 v[164:167], v192 offset:50176
	v_mul_f32_e32 v219, v215, v203
	v_cvt_pk_f16_f32 v220, v216, v217
	v_exp_f32_e32 v201, v113
	s_waitcnt lgkmcnt(2)
	v_mfma_f32_32x32x16_f16 v[0:15], a[84:87], v[168:171], v[0:15]
	ds_read_b128 v[168:171], v192 offset:51200
	v_cvt_pk_f16_f32 v221, v218, v219
	v_exp_f32_e32 v202, v114
	v_add_f32_e32 v200, 1.0, v200
	v_mfma_f32_32x32x16_f16 v[16:31], a[84:87], v[172:175], v[16:31]
	ds_read_b128 v[172:175], v192 offset:52224
	global_load_lds_dwordx4 v192, s[44:45] offset:3072 sc1
	v_exp_f32_e32 v203, v115
	v_add_f32_e32 v201, 1.0, v201
	v_add_f32_e32 v202, 1.0, v202
	v_mfma_f32_32x32x16_f16 v[0:15], a[88:91], v[176:179], v[0:15]
	ds_read_b128 v[176:179], v192 offset:53248
	v_exp_f32_e32 v204, v116
	v_add_f32_e32 v203, 1.0, v203
	v_mfma_f32_32x32x16_f16 v[16:31], a[88:91], v[180:183], v[16:31]
	ds_read_b128 v[180:183], v192 offset:54272
	v_exp_f32_e32 v205, v117
	v_add_f32_e32 v204, 1.0, v204
	v_mfma_f32_32x32x16_f16 v[0:15], a[92:95], v[184:187], v[0:15]
	ds_read_b128 v[184:187], v192 offset:55296
	v_exp_f32_e32 v206, v118
	v_add_f32_e32 v205, 1.0, v205
	v_mfma_f32_32x32x16_f16 v[16:31], a[92:95], v[188:191], v[16:31]
	ds_read_b128 v[188:191], v192 offset:56320
	s_mov_b32 m0, s59
	s_add_u32 s44, s34, 0x19000
	s_addc_u32 s45, s35, 0
	global_load_lds_dwordx4 v192, s[44:45] sc1
	v_exp_f32_e32 v207, v119
	v_add_f32_e32 v206, 1.0, v206
	s_waitcnt lgkmcnt(2)
	v_mfma_f32_32x32x16_f16 v[0:15], a[96:99], v[160:163], v[0:15]
	ds_read_b128 v[160:163], v192 offset:57344
	v_exp_f32_e32 v208, v120
	v_add_f32_e32 v207, 1.0, v207
	v_mfma_f32_32x32x16_f16 v[16:31], a[96:99], v[164:167], v[16:31]
	ds_read_b128 v[164:167], v192 offset:58368
	v_exp_f32_e32 v209, v121
	v_add_f32_e32 v208, 1.0, v208
	v_mfma_f32_32x32x16_f16 v[0:15], a[100:103], v[168:171], v[0:15]
	ds_read_b128 v[168:171], v192 offset:59392
	v_exp_f32_e32 v210, v122
	v_add_f32_e32 v209, 1.0, v209
	v_mfma_f32_32x32x16_f16 v[16:31], a[100:103], v[172:175], v[16:31]
	ds_read_b128 v[172:175], v192 offset:60416
	global_load_lds_dwordx4 v192, s[44:45] offset:1024 sc1
	v_exp_f32_e32 v211, v123
	v_add_f32_e32 v210, 1.0, v210
	v_mfma_f32_32x32x16_f16 v[0:15], a[104:107], v[176:179], v[0:15]
	ds_read_b128 v[176:179], v192 offset:61440
	v_exp_f32_e32 v212, v124
	v_add_f32_e32 v211, 1.0, v211
	v_mfma_f32_32x32x16_f16 v[16:31], a[104:107], v[180:183], v[16:31]
	ds_read_b128 v[180:183], v192 offset:62464
	v_exp_f32_e32 v213, v125
	v_add_f32_e32 v212, 1.0, v212
	s_waitcnt lgkmcnt(2)
	v_mfma_f32_32x32x16_f16 v[0:15], a[108:111], v[184:187], v[0:15]
	ds_read_b128 v[184:187], v192 offset:63488
	v_exp_f32_e32 v214, v126
	v_add_f32_e32 v213, 1.0, v213
	s_waitcnt vmcnt(14)
	v_mfma_f32_32x32x16_f16 v[16:31], a[108:111], v[188:191], v[16:31]
	ds_read_b128 v[188:191], v192 offset:64512
	global_load_lds_dwordx4 v192, s[44:45] offset:2048 sc1
	v_exp_f32_e32 v215, v127
	v_add_f32_e32 v214, 1.0, v214
	v_mfma_f32_32x32x2_f32 v[64:79], v248, v228, v[232:247]
	s_waitcnt vmcnt(7)
	s_barrier
	v_mfma_f32_32x32x16_f16 v[0:15], a[112:115], v[160:163], v[0:15]
	ds_read_b128 v[160:163], v193 offset:0
	v_add_f32_e32 v215, 1.0, v215
	v_rcp_f32_e32 v200, v200
	v_mfma_f32_32x32x2_f32 v[80:95], v248, v229, v[232:247]
	v_mfma_f32_32x32x16_f16 v[16:31], a[112:115], v[164:167], v[16:31]
	ds_read_b128 v[164:167], v193 offset:1024
	v_rcp_f32_e32 v201, v201
	v_mfma_f32_32x32x16_f16 v[0:15], a[116:119], v[168:171], v[0:15]
	ds_read_b128 v[168:171], v193 offset:2048
	v_rcp_f32_e32 v202, v202
	v_mfma_f32_32x32x16_f16 v[16:31], a[116:119], v[172:175], v[16:31]
	ds_read_b128 v[172:175], v193 offset:3072
	global_load_lds_dwordx4 v192, s[44:45] offset:3072 sc1
	v_rcp_f32_e32 v203, v203
	s_waitcnt lgkmcnt(2)
	v_mfma_f32_32x32x16_f16 v[0:15], a[120:123], v[176:179], v[0:15]
	ds_read_b128 v[176:179], v193 offset:4096
	v_rcp_f32_e32 v204, v204
	v_mfma_f32_32x32x16_f16 v[16:31], a[120:123], v[180:183], v[16:31]
	ds_read_b128 v[180:183], v193 offset:5120
	v_rcp_f32_e32 v205, v205
	v_mul_f32_e32 v204, v204, v156
	v_mfma_f32_32x32x16_f16 v[0:15], a[124:127], v[184:187], v[0:15]
	ds_read_b128 v[184:187], v193 offset:6144
	v_rcp_f32_e32 v206, v206
	v_mul_f32_e32 v205, v205, v157
	v_mfma_f32_32x32x16_f16 v[16:31], a[124:127], v[188:191], v[16:31]
	ds_read_b128 v[188:191], v193 offset:7168
	v_cmp_gt_u32_e32 vcc, 2, v251
	s_cbranch_vccnz .LE_tpoll17

.LE_htb23:
	v_exp_f32_e32 v203, v19
	v_mfma_f32_32x32x16_f16 v[32:47], a[88:91], v[176:179], v[32:47]
	ds_read_b128 v[176:179], v192 offset:53248
	v_exp_f32_e32 v204, v20
	v_add_f32_e32 v201, 1.0, v201
	v_add_f32_e32 v202, 1.0, v202
	v_mfma_f32_32x32x16_f16 v[48:63], a[88:91], v[180:183], v[48:63]
	ds_read_b128 v[180:183], v192 offset:54272
	v_exp_f32_e32 v205, v21
	v_add_f32_e32 v203, 1.0, v203
	v_add_f32_e32 v204, 1.0, v204
	v_mfma_f32_32x32x16_f16 v[32:47], a[92:95], v[184:187], v[32:47]
	ds_read_b128 v[184:187], v192 offset:55296
	v_exp_f32_e32 v206, v22
	v_add_f32_e32 v205, 1.0, v205
	v_mfma_f32_32x32x16_f16 v[48:63], a[92:95], v[188:191], v[48:63]
	ds_read_b128 v[188:191], v192 offset:56320
	s_mov_b32 m0, s59
	s_add_u32 s44, s34, 0x19000
	s_addc_u32 s45, s35, 0
	global_load_lds_dwordx4 v192, s[44:45] sc1
	v_exp_f32_e32 v207, v23
	v_add_f32_e32 v206, 1.0, v206
	s_waitcnt lgkmcnt(2)
	v_mfma_f32_32x32x16_f16 v[32:47], a[96:99], v[160:163], v[32:47]
	ds_read_b128 v[160:163], v192 offset:57344
	v_exp_f32_e32 v208, v24
	v_add_f32_e32 v207, 1.0, v207
	v_mfma_f32_32x32x16_f16 v[48:63], a[96:99], v[164:167], v[48:63]
	ds_read_b128 v[164:167], v192 offset:58368
	v_exp_f32_e32 v209, v25
	v_add_f32_e32 v208, 1.0, v208
	v_mfma_f32_32x32x16_f16 v[32:47], a[100:103], v[168:171], v[32:47]
	ds_read_b128 v[168:171], v192 offset:59392
	v_exp_f32_e32 v210, v26
	v_add_f32_e32 v209, 1.0, v209
	v_mfma_f32_32x32x16_f16 v[48:63], a[100:103], v[172:175], v[48:63]
	ds_read_b128 v[172:175], v192 offset:60416
	global_load_lds_dwordx4 v192, s[44:45] offset:1024 sc1
	v_exp_f32_e32 v211, v27
	v_add_f32_e32 v210, 1.0, v210
	v_mfma_f32_32x32x16_f16 v[32:47], a[104:107], v[176:179], v[32:47]
	ds_read_b128 v[176:179], v192 offset:61440
	v_exp_f32_e32 v212, v28
	v_add_f32_e32 v211, 1.0, v211
	v_mfma_f32_32x32x16_f16 v[48:63], a[104:107], v[180:183], v[48:63]
	ds_read_b128 v[180:183], v192 offset:62464
	v_exp_f32_e32 v213, v29
	v_add_f32_e32 v212, 1.0, v212
	s_waitcnt lgkmcnt(2)
	v_mfma_f32_32x32x16_f16 v[32:47], a[108:111], v[184:187], v[32:47]
	ds_read_b128 v[184:187], v192 offset:63488
	v_exp_f32_e32 v214, v30
	v_add_f32_e32 v213, 1.0, v213
	s_waitcnt vmcnt(14)
	v_mfma_f32_32x32x16_f16 v[48:63], a[108:111], v[188:191], v[48:63]
	ds_read_b128 v[188:191], v192 offset:64512
	global_load_lds_dwordx4 v192, s[44:45] offset:2048 sc1
	v_exp_f32_e32 v215, v31
	v_add_f32_e32 v214, 1.0, v214
	v_mfma_f32_32x32x2_f32 v[96:111], v248, v228, v[232:247]
	s_waitcnt vmcnt(7)
	s_barrier
	v_mfma_f32_32x32x16_f16 v[32:47], a[112:115], v[160:163], v[32:47]
	ds_read_b128 v[160:163], v193 offset:0
	v_add_f32_e32 v215, 1.0, v215
	v_rcp_f32_e32 v200, v200
	v_mfma_f32_32x32x2_f32 v[112:127], v248, v229, v[232:247]
	v_mfma_f32_32x32x16_f16 v[48:63], a[112:115], v[164:167], v[48:63]
	ds_read_b128 v[164:167], v193 offset:1024
	v_rcp_f32_e32 v201, v201
	v_mfma_f32_32x32x16_f16 v[32:47], a[116:119], v[168:171], v[32:47]
	ds_read_b128 v[168:171], v193 offset:2048
	v_rcp_f32_e32 v202, v202
	v_mfma_f32_32x32x16_f16 v[48:63], a[116:119], v[172:175], v[48:63]
	ds_read_b128 v[172:175], v193 offset:3072
	global_load_lds_dwordx4 v192, s[44:45] offset:3072 sc1
	v_rcp_f32_e32 v203, v203
	s_waitcnt lgkmcnt(2)
	v_mfma_f32_32x32x16_f16 v[32:47], a[120:123], v[176:179], v[32:47]
	ds_read_b128 v[176:179], v193 offset:4096
	v_rcp_f32_e32 v204, v204
	v_mfma_f32_32x32x16_f16 v[48:63], a[120:123], v[180:183], v[48:63]
	ds_read_b128 v[180:183], v193 offset:5120
	v_rcp_f32_e32 v205, v205
	v_mul_f32_e32 v204, v204, v132
	v_mfma_f32_32x32x16_f16 v[32:47], a[124:127], v[184:187], v[32:47]
	ds_read_b128 v[184:187], v193 offset:6144
	v_rcp_f32_e32 v206, v206
	v_mul_f32_e32 v205, v205, v133
	v_mfma_f32_32x32x16_f16 v[48:63], a[124:127], v[188:191], v[48:63]
	ds_read_b128 v[188:191], v193 offset:7168
	v_cmp_gt_u32_e32 vcc, 3, v251
	s_cbranch_vccnz .LE_tpoll25

.LE_htb33:
	v_exp_f32_e32 v203, v51
	v_mfma_f32_32x32x16_f16 v[64:79], a[88:91], v[176:179], v[64:79]
	ds_read_b128 v[176:179], v192 offset:53248
	v_exp_f32_e32 v204, v52
	v_add_f32_e32 v201, 1.0, v201
	v_add_f32_e32 v202, 1.0, v202
	v_mfma_f32_32x32x16_f16 v[80:95], a[88:91], v[180:183], v[80:95]
	ds_read_b128 v[180:183], v192 offset:54272
	v_exp_f32_e32 v205, v53
	v_add_f32_e32 v203, 1.0, v203
	v_add_f32_e32 v204, 1.0, v204
	v_mfma_f32_32x32x16_f16 v[64:79], a[92:95], v[184:187], v[64:79]
	ds_read_b128 v[184:187], v192 offset:55296
	v_exp_f32_e32 v206, v54
	v_add_f32_e32 v205, 1.0, v205
	v_mfma_f32_32x32x16_f16 v[80:95], a[92:95], v[188:191], v[80:95]
	ds_read_b128 v[188:191], v192 offset:56320
	s_mov_b32 m0, s59
	s_add_u32 s44, s34, 0x19000
	s_addc_u32 s45, s35, 0
	global_load_lds_dwordx4 v192, s[44:45] sc1
	v_exp_f32_e32 v207, v55
	v_add_f32_e32 v206, 1.0, v206
	s_waitcnt lgkmcnt(2)
	v_mfma_f32_32x32x16_f16 v[64:79], a[96:99], v[160:163], v[64:79]
	ds_read_b128 v[160:163], v192 offset:57344
	v_exp_f32_e32 v208, v56
	v_add_f32_e32 v207, 1.0, v207
	v_mfma_f32_32x32x16_f16 v[80:95], a[96:99], v[164:167], v[80:95]
	ds_read_b128 v[164:167], v192 offset:58368
	v_exp_f32_e32 v209, v57
	v_add_f32_e32 v208, 1.0, v208
	v_mfma_f32_32x32x16_f16 v[64:79], a[100:103], v[168:171], v[64:79]
	ds_read_b128 v[168:171], v192 offset:59392
	v_exp_f32_e32 v210, v58
	v_add_f32_e32 v209, 1.0, v209
	v_mfma_f32_32x32x16_f16 v[80:95], a[100:103], v[172:175], v[80:95]
	ds_read_b128 v[172:175], v192 offset:60416
	global_load_lds_dwordx4 v192, s[44:45] offset:1024 sc1
	v_exp_f32_e32 v211, v59
	v_add_f32_e32 v210, 1.0, v210
	v_mfma_f32_32x32x16_f16 v[64:79], a[104:107], v[176:179], v[64:79]
	ds_read_b128 v[176:179], v192 offset:61440
	v_exp_f32_e32 v212, v60
	v_add_f32_e32 v211, 1.0, v211
	v_mfma_f32_32x32x16_f16 v[80:95], a[104:107], v[180:183], v[80:95]
	ds_read_b128 v[180:183], v192 offset:62464
	v_exp_f32_e32 v213, v61
	v_add_f32_e32 v212, 1.0, v212
	s_waitcnt lgkmcnt(2)
	v_mfma_f32_32x32x16_f16 v[64:79], a[108:111], v[184:187], v[64:79]
	ds_read_b128 v[184:187], v192 offset:63488
	v_exp_f32_e32 v214, v62
	v_add_f32_e32 v213, 1.0, v213
	s_waitcnt vmcnt(14)
	v_mfma_f32_32x32x16_f16 v[80:95], a[108:111], v[188:191], v[80:95]
	ds_read_b128 v[188:191], v192 offset:64512
	global_load_lds_dwordx4 v192, s[44:45] offset:2048 sc1
	v_exp_f32_e32 v215, v63
	v_add_f32_e32 v214, 1.0, v214
	v_mfma_f32_32x32x2_f32 v[0:15], v248, v228, v[232:247]
	s_waitcnt vmcnt(7)
	s_barrier
	v_mfma_f32_32x32x16_f16 v[64:79], a[112:115], v[160:163], v[64:79]
	ds_read_b128 v[160:163], v193 offset:0
	v_add_f32_e32 v215, 1.0, v215
	v_rcp_f32_e32 v200, v200
	v_mfma_f32_32x32x2_f32 v[16:31], v248, v229, v[232:247]
	v_mfma_f32_32x32x16_f16 v[80:95], a[112:115], v[164:167], v[80:95]
	ds_read_b128 v[164:167], v193 offset:1024
	v_rcp_f32_e32 v201, v201
	v_mfma_f32_32x32x16_f16 v[64:79], a[116:119], v[168:171], v[64:79]
	ds_read_b128 v[168:171], v193 offset:2048
	v_rcp_f32_e32 v202, v202
	v_mfma_f32_32x32x16_f16 v[80:95], a[116:119], v[172:175], v[80:95]
	ds_read_b128 v[172:175], v193 offset:3072
	global_load_lds_dwordx4 v192, s[44:45] offset:3072 sc1
	v_rcp_f32_e32 v203, v203
	s_waitcnt lgkmcnt(2)
	v_mfma_f32_32x32x16_f16 v[64:79], a[120:123], v[176:179], v[64:79]
	ds_read_b128 v[176:179], v193 offset:4096
	v_rcp_f32_e32 v204, v204
	v_mfma_f32_32x32x16_f16 v[80:95], a[120:123], v[180:183], v[80:95]
	ds_read_b128 v[180:183], v193 offset:5120
	v_rcp_f32_e32 v205, v205
	v_mul_f32_e32 v204, v204, v140
	v_mfma_f32_32x32x16_f16 v[64:79], a[124:127], v[184:187], v[64:79]
	ds_read_b128 v[184:187], v193 offset:6144
	v_rcp_f32_e32 v206, v206
	v_mul_f32_e32 v205, v205, v141
	v_mfma_f32_32x32x16_f16 v[80:95], a[124:127], v[188:191], v[80:95]
	ds_read_b128 v[188:191], v193 offset:7168
	v_cmp_gt_u32_e32 vcc, 4, v251
	s_cbranch_vccnz .LE_tpoll35

.LE_htb43:
	v_exp_f32_e32 v203, v83
	v_mfma_f32_32x32x16_f16 v[96:111], a[88:91], v[176:179], v[96:111]
	ds_read_b128 v[176:179], v192 offset:53248
	v_exp_f32_e32 v204, v84
	v_add_f32_e32 v201, 1.0, v201
	v_add_f32_e32 v202, 1.0, v202
	v_mfma_f32_32x32x16_f16 v[112:127], a[88:91], v[180:183], v[112:127]
	ds_read_b128 v[180:183], v192 offset:54272
	v_exp_f32_e32 v205, v85
	v_add_f32_e32 v203, 1.0, v203
	v_add_f32_e32 v204, 1.0, v204
	v_mfma_f32_32x32x16_f16 v[96:111], a[92:95], v[184:187], v[96:111]
	ds_read_b128 v[184:187], v192 offset:55296
	v_exp_f32_e32 v206, v86
	v_add_f32_e32 v205, 1.0, v205
	v_mfma_f32_32x32x16_f16 v[112:127], a[92:95], v[188:191], v[112:127]
	ds_read_b128 v[188:191], v192 offset:56320
	s_mov_b32 m0, s59
	s_add_u32 s44, s34, 0x19000
	s_addc_u32 s45, s35, 0
	global_load_lds_dwordx4 v192, s[44:45] sc1
	v_exp_f32_e32 v207, v87
	v_add_f32_e32 v206, 1.0, v206
	s_waitcnt lgkmcnt(2)
	v_mfma_f32_32x32x16_f16 v[96:111], a[96:99], v[160:163], v[96:111]
	ds_read_b128 v[160:163], v192 offset:57344
	v_exp_f32_e32 v208, v88
	v_add_f32_e32 v207, 1.0, v207
	v_mfma_f32_32x32x16_f16 v[112:127], a[96:99], v[164:167], v[112:127]
	ds_read_b128 v[164:167], v192 offset:58368
	v_exp_f32_e32 v209, v89
	v_add_f32_e32 v208, 1.0, v208
	v_mfma_f32_32x32x16_f16 v[96:111], a[100:103], v[168:171], v[96:111]
	ds_read_b128 v[168:171], v192 offset:59392
	v_exp_f32_e32 v210, v90
	v_add_f32_e32 v209, 1.0, v209
	v_mfma_f32_32x32x16_f16 v[112:127], a[100:103], v[172:175], v[112:127]
	ds_read_b128 v[172:175], v192 offset:60416
	global_load_lds_dwordx4 v192, s[44:45] offset:1024 sc1
	v_exp_f32_e32 v211, v91
	v_add_f32_e32 v210, 1.0, v210
	v_mfma_f32_32x32x16_f16 v[96:111], a[104:107], v[176:179], v[96:111]
	ds_read_b128 v[176:179], v192 offset:61440
	v_exp_f32_e32 v212, v92
	v_add_f32_e32 v211, 1.0, v211
	v_mfma_f32_32x32x16_f16 v[112:127], a[104:107], v[180:183], v[112:127]
	ds_read_b128 v[180:183], v192 offset:62464
	v_exp_f32_e32 v213, v93
	v_add_f32_e32 v212, 1.0, v212
	s_waitcnt lgkmcnt(2)
	v_mfma_f32_32x32x16_f16 v[96:111], a[108:111], v[184:187], v[96:111]
	ds_read_b128 v[184:187], v192 offset:63488
	v_exp_f32_e32 v214, v94
	v_add_f32_e32 v213, 1.0, v213
	s_waitcnt vmcnt(14)
	v_mfma_f32_32x32x16_f16 v[112:127], a[108:111], v[188:191], v[112:127]
	ds_read_b128 v[188:191], v192 offset:64512
	global_load_lds_dwordx4 v192, s[44:45] offset:2048 sc1
	v_exp_f32_e32 v215, v95
	v_add_f32_e32 v214, 1.0, v214
	v_mfma_f32_32x32x2_f32 v[32:47], v248, v228, v[232:247]
	s_waitcnt vmcnt(7)
	s_barrier
	v_mfma_f32_32x32x16_f16 v[96:111], a[112:115], v[160:163], v[96:111]
	ds_read_b128 v[160:163], v193 offset:0
	v_add_f32_e32 v215, 1.0, v215
	v_rcp_f32_e32 v200, v200
	v_mfma_f32_32x32x2_f32 v[48:63], v248, v229, v[232:247]
	v_mfma_f32_32x32x16_f16 v[112:127], a[112:115], v[164:167], v[112:127]
	ds_read_b128 v[164:167], v193 offset:1024
	v_rcp_f32_e32 v201, v201
	v_mfma_f32_32x32x16_f16 v[96:111], a[116:119], v[168:171], v[96:111]
	ds_read_b128 v[168:171], v193 offset:2048
	v_rcp_f32_e32 v202, v202
	v_mfma_f32_32x32x16_f16 v[112:127], a[116:119], v[172:175], v[112:127]
	ds_read_b128 v[172:175], v193 offset:3072
	global_load_lds_dwordx4 v192, s[44:45] offset:3072 sc1
	v_rcp_f32_e32 v203, v203
	s_waitcnt lgkmcnt(2)
	v_mfma_f32_32x32x16_f16 v[96:111], a[120:123], v[176:179], v[96:111]
	ds_read_b128 v[176:179], v193 offset:4096
	v_rcp_f32_e32 v204, v204
	v_mfma_f32_32x32x16_f16 v[112:127], a[120:123], v[180:183], v[112:127]
	ds_read_b128 v[180:183], v193 offset:5120
	v_rcp_f32_e32 v205, v205
	v_mul_f32_e32 v204, v204, v148
	v_mfma_f32_32x32x16_f16 v[96:111], a[124:127], v[184:187], v[96:111]
	ds_read_b128 v[184:187], v193 offset:6144
	v_rcp_f32_e32 v206, v206
	v_mul_f32_e32 v205, v205, v149
	v_mfma_f32_32x32x16_f16 v[112:127], a[124:127], v[188:191], v[112:127]
	ds_read_b128 v[188:191], v193 offset:7168
	v_cmp_gt_u32_e32 vcc, 1, v251
	s_cbranch_vccnz .LE_tpoll45

.LD_loop12:
	s_sub_u32 s71, s33, 1
	s_add_u32 s61, s33, 1
	s_min_u32 s61, s61, s60
	s_and_b32 s64, s71, 1
	s_lshl_b32 s64, s64, 22
	s_add_u32 s64, s64, s50
	s_add_u32 s64, s64, 0x60000
	s_add_u32 s36, s6, s64
	s_addc_u32 s37, s7, 0
	s_lshl_b32 s64, s71, 3
	s_add_u32 s64, s64, s29
	s_lshl_b32 s64, s64, 5
	s_add_u32 s64, s64, s30
	s_lshl_b32 s64, s64, 2
	s_add_u32 s40, s8, s64
	s_addc_u32 s41, s9, 0
	s_lshl_b32 s64, s71, 19
	s_add_u32 s64, s64, 0x600
	s_add_u32 s72, s62, s64
	s_addc_u32 s73, s63, 0
	s_nop 3
	s_waitcnt lgkmcnt(2)
	v_mfma_f32_32x32x16_f16 v[0:15], a[0:3], v[160:163], v[0:15]
	ds_read_b128 v[160:163], v192 offset:8192
	v_exp_f32_e32 v200, v96
	v_mfma_f32_32x32x16_f16 v[16:31], a[0:3], v[164:167], v[16:31]
	ds_read_b128 v[164:167], v192 offset:9216
	s_lshl_b32 s64, s71, 3
	s_add_u32 s64, s64, s29
	s_lshl_b32 s64, s64, 7
	s_add_u32 s38, s8, s64
	s_addc_u32 s39, s9, 0
	global_load_dword v251, v196, s[38:39] sc1
	v_exp_f32_e32 v201, v97
	v_add_f32_e32 v200, 1.0, v200
	v_mfma_f32_32x32x16_f16 v[0:15], a[4:7], v[168:171], v[0:15]
	ds_read_b128 v[168:171], v192 offset:10240
	v_exp_f32_e32 v202, v98
	v_add_f32_e32 v201, 1.0, v201
	v_mfma_f32_32x32x16_f16 v[16:31], a[4:7], v[172:175], v[16:31]
	ds_read_b128 v[172:175], v192 offset:11264
	global_load_lds_dwordx4 v192, s[44:45] offset:1024 sc1
	v_exp_f32_e32 v203, v99
	v_add_f32_e32 v202, 1.0, v202
	v_mfma_f32_32x32x16_f16 v[0:15], a[8:11], v[176:179], v[0:15]
	ds_read_b128 v[176:179], v192 offset:12288
	v_exp_f32_e32 v204, v100
	v_add_f32_e32 v203, 1.0, v203
	v_mfma_f32_32x32x16_f16 v[16:31], a[8:11], v[180:183], v[16:31]
	ds_read_b128 v[180:183], v192 offset:13312
	v_exp_f32_e32 v205, v101
	v_add_f32_e32 v204, 1.0, v204
	s_waitcnt lgkmcnt(2)
	v_mfma_f32_32x32x16_f16 v[0:15], a[12:15], v[184:187], v[0:15]
	ds_read_b128 v[184:187], v192 offset:14336
	v_exp_f32_e32 v206, v102
	v_add_f32_e32 v205, 1.0, v205
	v_mfma_f32_32x32x16_f16 v[16:31], a[12:15], v[188:191], v[16:31]
	ds_read_b128 v[188:191], v192 offset:15360
	global_load_lds_dwordx4 v192, s[44:45] offset:2048 sc1
	v_exp_f32_e32 v207, v103
	v_add_f32_e32 v206, 1.0, v206
	v_mfma_f32_32x32x16_f16 v[0:15], a[16:19], v[160:163], v[0:15]
	ds_read_b128 v[160:163], v192 offset:16384
	v_exp_f32_e32 v208, v104
	v_add_f32_e32 v207, 1.0, v207
	v_mfma_f32_32x32x16_f16 v[16:31], a[16:19], v[164:167], v[16:31]
	ds_read_b128 v[164:167], v192 offset:17408
	v_exp_f32_e32 v209, v105
	v_add_f32_e32 v208, 1.0, v208
	v_mfma_f32_32x32x16_f16 v[0:15], a[20:23], v[168:171], v[0:15]
	ds_read_b128 v[168:171], v192 offset:18432
	v_exp_f32_e32 v210, v106
	v_add_f32_e32 v209, 1.0, v209
	v_mfma_f32_32x32x16_f16 v[16:31], a[20:23], v[172:175], v[16:31]
	ds_read_b128 v[172:175], v192 offset:19456
	global_load_lds_dwordx4 v192, s[44:45] offset:3072 sc1
	v_exp_f32_e32 v211, v107
	v_add_f32_e32 v210, 1.0, v210
	s_waitcnt lgkmcnt(2)
	v_mfma_f32_32x32x16_f16 v[0:15], a[24:27], v[176:179], v[0:15]
	ds_read_b128 v[176:179], v192 offset:20480
	v_exp_f32_e32 v212, v108
	v_add_f32_e32 v211, 1.0, v211
	v_mfma_f32_32x32x16_f16 v[16:31], a[24:27], v[180:183], v[16:31]
	ds_read_b128 v[180:183], v192 offset:21504
	v_exp_f32_e32 v213, v109
	v_add_f32_e32 v212, 1.0, v212
	v_mfma_f32_32x32x16_f16 v[0:15], a[28:31], v[184:187], v[0:15]
	ds_read_b128 v[184:187], v192 offset:22528
	v_exp_f32_e32 v214, v110
	v_add_f32_e32 v213, 1.0, v213
	v_mfma_f32_32x32x16_f16 v[16:31], a[28:31], v[188:191], v[16:31]
	ds_read_b128 v[188:191], v192 offset:23552
	s_mov_b32 m0, s57
	s_add_u32 s44, s34, 0x11000
	s_addc_u32 s45, s35, 0
	global_load_lds_dwordx4 v192, s[44:45] sc1
	v_exp_f32_e32 v215, v111
	v_add_f32_e32 v214, 1.0, v214
	v_mfma_f32_32x32x16_f16 v[0:15], a[32:35], v[160:163], v[0:15]
	ds_read_b128 v[160:163], v192 offset:24576
	v_add_f32_e32 v215, 1.0, v215
	v_rcp_f32_e32 v200, v200
	v_mfma_f32_32x32x16_f16 v[16:31], a[32:35], v[164:167], v[16:31]
	ds_read_b128 v[164:167], v192 offset:25600
	v_rcp_f32_e32 v201, v201
	s_waitcnt lgkmcnt(2)
	v_mfma_f32_32x32x16_f16 v[0:15], a[36:39], v[168:171], v[0:15]
	ds_read_b128 v[168:171], v192 offset:26624
	v_rcp_f32_e32 v202, v202
	v_mfma_f32_32x32x16_f16 v[16:31], a[36:39], v[172:175], v[16:31]
	ds_read_b128 v[172:175], v192 offset:27648
	global_load_lds_dwordx4 v192, s[44:45] offset:1024 sc1
	v_rcp_f32_e32 v203, v203
	v_mfma_f32_32x32x16_f16 v[0:15], a[40:43], v[176:179], v[0:15]
	ds_read_b128 v[176:179], v192 offset:28672
	v_rcp_f32_e32 v204, v204
	v_mfma_f32_32x32x16_f16 v[16:31], a[40:43], v[180:183], v[16:31]
	ds_read_b128 v[180:183], v192 offset:29696
	v_rcp_f32_e32 v205, v205
	v_mul_f32_e32 v204, v204, v152
	v_mfma_f32_32x32x16_f16 v[0:15], a[44:47], v[184:187], v[0:15]
	ds_read_b128 v[184:187], v192 offset:30720
	v_rcp_f32_e32 v206, v206
	v_mul_f32_e32 v205, v205, v153
	v_mfma_f32_32x32x16_f16 v[16:31], a[44:47], v[188:191], v[16:31]
	ds_read_b128 v[188:191], v192 offset:31744
	global_load_lds_dwordx4 v192, s[44:45] offset:2048 sc1
	v_rcp_f32_e32 v207, v207
	v_mul_f32_e32 v206, v206, v154
	s_waitcnt vmcnt(8)
	s_barrier
	s_waitcnt lgkmcnt(2)
	v_mfma_f32_32x32x16_f16 v[0:15], a[48:51], v[160:163], v[0:15]
	ds_read_b128 v[160:163], v192 offset:32768
	v_rcp_f32_e32 v208, v208
	v_mul_f32_e32 v207, v207, v155
	v_mfma_f32_32x32x16_f16 v[16:31], a[48:51], v[164:167], v[16:31]
	ds_read_b128 v[164:167], v192 offset:33792
	v_rcp_f32_e32 v209, v209
	v_fmamk_f32 v208, v208, 0xc0b8aa3b, v198
	v_mfma_f32_32x32x16_f16 v[0:15], a[52:55], v[168:171], v[0:15]
	ds_read_b128 v[168:171], v192 offset:34816
	v_rcp_f32_e32 v210, v210
	v_fmamk_f32 v209, v209, 0xc0b8aa3b, v198
	v_fma_f32 v152, v200, v208, v204
	v_mfma_f32_32x32x16_f16 v[16:31], a[52:55], v[172:175], v[16:31]
	ds_read_b128 v[172:175], v192 offset:35840
	global_load_lds_dwordx4 v192, s[44:45] offset:3072 sc1
	v_rcp_f32_e32 v211, v211
	v_fmamk_f32 v210, v210, 0xc0b8aa3b, v198
	v_fma_f32 v153, v201, v209, v205
	v_mfma_f32_32x32x16_f16 v[0:15], a[56:59], v[176:179], v[0:15]
	ds_read_b128 v[176:179], v192 offset:36864
	v_rcp_f32_e32 v212, v212
	v_fmamk_f32 v211, v211, 0xc0b8aa3b, v198
	v_fma_f32 v154, v202, v210, v206
	v_mfma_f32_32x32x16_f16 v[16:31], a[56:59], v[180:183], v[16:31]
	ds_read_b128 v[180:183], v192 offset:37888
	v_rcp_f32_e32 v213, v213
	v_fma_f32 v155, v203, v211, v207
	s_waitcnt lgkmcnt(2)
	v_mfma_f32_32x32x16_f16 v[0:15], a[60:63], v[184:187], v[0:15]
	ds_read_b128 v[184:187], v192 offset:38912
	v_rcp_f32_e32 v214, v214
	v_mfma_f32_32x32x16_f16 v[16:31], a[60:63], v[188:191], v[16:31]
	ds_read_b128 v[188:191], v192 offset:39936
	s_mov_b32 m0, s58
	s_add_u32 s44, s34, 0x18000
	s_addc_u32 s45, s35, 0
	global_load_lds_dwordx4 v192, s[44:45] sc1
	v_rcp_f32_e32 v215, v215
	v_mfma_f32_32x32x16_f16 v[0:15], a[64:67], v[160:163], v[0:15]
	ds_read_b128 v[160:163], v192 offset:40960
	v_exp_f32_e32 v200, v152
	v_mfma_f32_32x32x16_f16 v[16:31], a[64:67], v[164:167], v[16:31]
	ds_read_b128 v[164:167], v192 offset:41984
	v_exp_f32_e32 v201, v153
	v_add_f32_e32 v200, 1.0, v200
	v_mfma_f32_32x32x16_f16 v[0:15], a[68:71], v[168:171], v[0:15]
	ds_read_b128 v[168:171], v192 offset:43008
	v_exp_f32_e32 v202, v154
	v_add_f32_e32 v201, 1.0, v201
	v_mfma_f32_32x32x16_f16 v[16:31], a[68:71], v[172:175], v[16:31]
	ds_read_b128 v[172:175], v192 offset:44032
	global_load_lds_dwordx4 v192, s[44:45] offset:1024 sc1
	v_exp_f32_e32 v203, v155
	v_add_f32_e32 v202, 1.0, v202
	s_waitcnt lgkmcnt(2)
	v_mfma_f32_32x32x16_f16 v[0:15], a[72:75], v[176:179], v[0:15]
	ds_read_b128 v[176:179], v192 offset:45056
	v_add_f32_e32 v203, 1.0, v203
	v_rcp_f32_e32 v200, v200
	v_mfma_f32_32x32x16_f16 v[16:31], a[72:75], v[180:183], v[16:31]
	ds_read_b128 v[180:183], v192 offset:46080
	v_rcp_f32_e32 v201, v201
	v_fma_f32 v200, v200, 2.0, -1.0
	v_mfma_f32_32x32x16_f16 v[0:15], a[76:79], v[184:187], v[0:15]
	ds_read_b128 v[184:187], v192 offset:47104
	v_rcp_f32_e32 v202, v202
	v_fma_f32 v201, v201, 2.0, -1.0
	v_mul_f32_e32 v216, v212, v200
	v_mfma_f32_32x32x16_f16 v[16:31], a[76:79], v[188:191], v[16:31]
	ds_read_b128 v[188:191], v192 offset:48128
	global_load_lds_dwordx4 v192, s[44:45] offset:2048 sc1
	v_rcp_f32_e32 v203, v203
	v_fma_f32 v202, v202, 2.0, -1.0
	v_mul_f32_e32 v217, v213, v201
	v_mfma_f32_32x32x16_f16 v[0:15], a[80:83], v[160:163], v[0:15]
	ds_read_b128 v[160:163], v192 offset:49152
	v_fma_f32 v203, v203, 2.0, -1.0
	v_mul_f32_e32 v218, v214, v202
	v_exp_f32_e32 v200, v112
	v_mfma_f32_32x32x16_f16 v[16:31], a[80:83], v[164:167], v[16:31]
	ds_read_b128 v[164:167], v192 offset:50176
	v_mul_f32_e32 v219, v215, v203
	v_mul_f32_e32 v236, v216, v228
	v_exp_f32_e32 v201, v113
	s_waitcnt lgkmcnt(2)
	v_mfma_f32_32x32x16_f16 v[0:15], a[84:87], v[168:171], v[0:15]
	ds_read_b128 v[168:171], v192 offset:51200
	v_mul_f32_e32 v237, v216, v232
	v_fmac_f32_e32 v236, v217, v229
	v_exp_f32_e32 v202, v114
	v_mfma_f32_32x32x16_f16 v[16:31], a[84:87], v[172:175], v[16:31]
	ds_read_b128 v[172:175], v192 offset:52224
	global_load_lds_dwordx4 v192, s[44:45] offset:3072 sc1
	v_fmac_f32_e32 v237, v217, v233
	v_fmac_f32_e32 v236, v218, v230
	v_exp_f32_e32 v203, v115
	v_mfma_f32_32x32x16_f16 v[0:15], a[88:91], v[176:179], v[0:15]
	ds_read_b128 v[176:179], v192 offset:53248
	v_fmac_f32_e32 v237, v218, v234
	v_fmac_f32_e32 v236, v219, v231
	v_exp_f32_e32 v204, v116
	v_mfma_f32_32x32x16_f16 v[16:31], a[88:91], v[180:183], v[16:31]
	ds_read_b128 v[180:183], v192 offset:54272
	v_fmac_f32_e32 v237, v219, v235
	v_mov_b32_e32 v238, v236
	v_exp_f32_e32 v205, v117
	v_mfma_f32_32x32x16_f16 v[0:15], a[92:95], v[184:187], v[0:15]
	ds_read_b128 v[184:187], v192 offset:55296
	v_mov_b32_e32 v240, v237
	v_cvt_pk_f16_f32 v220, v216, v217
	v_exp_f32_e32 v206, v118
	v_mfma_f32_32x32x16_f16 v[16:31], a[92:95], v[188:191], v[16:31]
	ds_read_b128 v[188:191], v192 offset:56320
	s_mov_b32 m0, s59
	s_add_u32 s44, s34, 0x19000
	s_addc_u32 s45, s35, 0
	global_load_lds_dwordx4 v192, s[44:45] sc1
	v_permlane32_swap_b32_e32 v236, v238
	v_permlane32_swap_b32_e32 v237, v240
	v_add_f32_e32 v238, v236, v238
	v_add_f32_e32 v239, v237, v240
	ds_write_b64 v248, v[238:239] offset:1536
	v_exp_f32_e32 v207, v119
	s_waitcnt lgkmcnt(3)
	v_mfma_f32_32x32x16_f16 v[0:15], a[96:99], v[160:163], v[0:15]
	ds_read_b128 v[160:163], v192 offset:57344
	v_cvt_pk_f16_f32 v221, v218, v219
	v_exp_f32_e32 v208, v120
	v_add_f32_e32 v200, 1.0, v200
	v_mfma_f32_32x32x16_f16 v[16:31], a[96:99], v[164:167], v[16:31]
	ds_read_b128 v[164:167], v192 offset:58368
	v_exp_f32_e32 v209, v121
	v_add_f32_e32 v201, 1.0, v201
	v_add_f32_e32 v202, 1.0, v202
	v_mfma_f32_32x32x16_f16 v[0:15], a[100:103], v[168:171], v[0:15]
	ds_read_b128 v[168:171], v192 offset:59392
	v_exp_f32_e32 v210, v122
	v_add_f32_e32 v203, 1.0, v203
	v_add_f32_e32 v204, 1.0, v204
	v_mfma_f32_32x32x16_f16 v[16:31], a[100:103], v[172:175], v[16:31]
	ds_read_b128 v[172:175], v192 offset:60416
	global_load_lds_dwordx4 v192, s[44:45] offset:1024 sc1
	v_exp_f32_e32 v211, v123
	v_add_f32_e32 v205, 1.0, v205
	v_add_f32_e32 v206, 1.0, v206
	v_mfma_f32_32x32x16_f16 v[0:15], a[104:107], v[176:179], v[0:15]
	ds_read_b128 v[176:179], v192 offset:61440
	v_exp_f32_e32 v212, v124
	v_add_f32_e32 v207, 1.0, v207
	v_add_f32_e32 v208, 1.0, v208
	v_mfma_f32_32x32x16_f16 v[16:31], a[104:107], v[180:183], v[16:31]
	ds_read_b128 v[180:183], v192 offset:62464
	v_exp_f32_e32 v213, v125
	v_add_f32_e32 v209, 1.0, v209
	v_add_f32_e32 v210, 1.0, v210
	s_waitcnt lgkmcnt(2)
	v_mfma_f32_32x32x16_f16 v[0:15], a[108:111], v[184:187], v[0:15]
	ds_read_b128 v[184:187], v192 offset:63488
	v_exp_f32_e32 v214, v126
	v_add_f32_e32 v211, 1.0, v211
	v_add_f32_e32 v212, 1.0, v212
	s_add_u32 s46, s42, 0x4000
	s_addc_u32 s47, s43, 0
	global_load_dwordx4 v[64:67], v192, s[46:47] offset:0
	v_mfma_f32_32x32x16_f16 v[16:31], a[108:111], v[188:191], v[16:31]
	ds_read_b128 v[188:191], v192 offset:64512
	global_load_lds_dwordx4 v192, s[44:45] offset:2048 sc1
	v_exp_f32_e32 v215, v127
	v_add_f32_e32 v213, 1.0, v213
	v_add_f32_e32 v214, 1.0, v214
	global_load_dwordx4 v[68:71], v192, s[46:47] offset:1024
	global_load_dwordx4 v[72:75], v192, s[46:47] offset:2048
	s_waitcnt vmcnt(10)
	s_barrier
	v_mfma_f32_32x32x16_f16 v[0:15], a[112:115], v[160:163], v[0:15]
	ds_read_b128 v[160:163], v193 offset:0
	v_add_f32_e32 v215, 1.0, v215
	v_rcp_f32_e32 v200, v200
	global_load_dwordx4 v[76:79], v192, s[46:47] offset:3072
	s_add_u32 s46, s42, 0x5000
	s_addc_u32 s47, s43, 0
	v_mfma_f32_32x32x16_f16 v[16:31], a[112:115], v[164:167], v[16:31]
	ds_read_b128 v[164:167], v193 offset:1024
	v_rcp_f32_e32 v201, v201
	global_load_dwordx4 v[80:83], v192, s[46:47] offset:0
	global_load_dwordx4 v[84:87], v192, s[46:47] offset:1024
	v_mfma_f32_32x32x16_f16 v[0:15], a[116:119], v[168:171], v[0:15]
	ds_read_b128 v[168:171], v193 offset:2048
	v_rcp_f32_e32 v202, v202
	global_load_dwordx4 v[88:91], v192, s[46:47] offset:2048
	global_load_dwordx4 v[92:95], v192, s[46:47] offset:3072
	v_mfma_f32_32x32x16_f16 v[16:31], a[116:119], v[172:175], v[16:31]
	ds_read_b128 v[172:175], v193 offset:3072
	global_load_lds_dwordx4 v192, s[44:45] offset:3072 sc1
	v_rcp_f32_e32 v203, v203
	s_waitcnt lgkmcnt(2)
	v_mfma_f32_32x32x16_f16 v[0:15], a[120:123], v[176:179], v[0:15]
	ds_read_b128 v[176:179], v193 offset:4096
	v_rcp_f32_e32 v204, v204
	v_mfma_f32_32x32x16_f16 v[16:31], a[120:123], v[180:183], v[16:31]
	ds_read_b128 v[180:183], v193 offset:5120
	v_rcp_f32_e32 v205, v205
	v_mul_f32_e32 v204, v204, v156
	v_mfma_f32_32x32x16_f16 v[0:15], a[124:127], v[184:187], v[0:15]
	ds_read_b128 v[184:187], v193 offset:6144
	v_rcp_f32_e32 v206, v206
	v_mul_f32_e32 v205, v205, v157
	v_mfma_f32_32x32x16_f16 v[16:31], a[124:127], v[188:191], v[16:31]
	ds_read_b128 v[188:191], v193 offset:7168
	v_cmp_gt_u32_e32 vcc, 2, v251
	s_cbranch_vccnz .LD_tpoll17
.LD_tok16:
	s_and_b32 s64, s71, 1
	s_lshl_b32 s64, s64, 22
	s_add_u32 s64, s64, s49
	s_add_u32 s64, s64, 0x20000
	s_add_u32 s34, s6, s64
	s_addc_u32 s35, s7, 0
	s_mov_b32 m0, s52
	s_add_u32 s44, s34, 0x0
	s_addc_u32 s45, s35, 0
	global_load_lds_dwordx4 v192, s[44:45] sc1
	v_rcp_f32_e32 v207, v207
	v_mul_f32_e32 v206, v206, v158
	v_mfma_f32_32x32x16_f16 v[0:15], a[128:131], v[160:163], v[0:15]
	ds_read_b128 v[160:163], v193 offset:8192
	v_rcp_f32_e32 v208, v208
	v_mul_f32_e32 v207, v207, v159
	v_mfma_f32_32x32x16_f16 v[16:31], a[128:131], v[164:167], v[16:31]
	ds_read_b128 v[164:167], v193 offset:9216
	v_rcp_f32_e32 v209, v209
	v_fmamk_f32 v208, v208, 0xc0b8aa3b, v198
	s_waitcnt lgkmcnt(2)
	v_mfma_f32_32x32x16_f16 v[0:15], a[132:135], v[168:171], v[0:15]
	ds_read_b128 v[168:171], v193 offset:10240
	v_rcp_f32_e32 v210, v210
	v_fmamk_f32 v209, v209, 0xc0b8aa3b, v198
	v_fma_f32 v156, v200, v208, v204
	v_mfma_f32_32x32x16_f16 v[16:31], a[132:135], v[172:175], v[16:31]
	ds_read_b128 v[172:175], v193 offset:11264
	global_load_lds_dwordx4 v192, s[44:45] offset:1024 sc1
	v_rcp_f32_e32 v211, v211
	v_fmamk_f32 v210, v210, 0xc0b8aa3b, v198
	v_fma_f32 v157, v201, v209, v205
	v_mfma_f32_32x32x16_f16 v[0:15], a[136:139], v[176:179], v[0:15]
	ds_read_b128 v[176:179], v193 offset:12288
	v_rcp_f32_e32 v212, v212
	v_fmamk_f32 v211, v211, 0xc0b8aa3b, v198
	v_fma_f32 v158, v202, v210, v206
	v_mfma_f32_32x32x16_f16 v[16:31], a[136:139], v[180:183], v[16:31]
	ds_read_b128 v[180:183], v193 offset:13312
	v_rcp_f32_e32 v213, v213
	v_fma_f32 v159, v203, v211, v207
	v_mfma_f32_32x32x16_f16 v[0:15], a[140:143], v[184:187], v[0:15]
	ds_read_b128 v[184:187], v193 offset:14336
	v_rcp_f32_e32 v214, v214
	v_mfma_f32_32x32x16_f16 v[16:31], a[140:143], v[188:191], v[16:31]
	ds_read_b128 v[188:191], v193 offset:15360
	global_load_lds_dwordx4 v192, s[44:45] offset:2048 sc1
	v_rcp_f32_e32 v215, v215
	s_waitcnt lgkmcnt(2)
	v_mfma_f32_32x32x16_f16 v[0:15], a[144:147], v[160:163], v[0:15]
	ds_read_b128 v[160:163], v193 offset:16384
	v_exp_f32_e32 v200, v156
	v_mfma_f32_32x32x16_f16 v[16:31], a[144:147], v[164:167], v[16:31]
	ds_read_b128 v[164:167], v193 offset:17408
	v_exp_f32_e32 v201, v157
	v_add_f32_e32 v200, 1.0, v200
	v_mfma_f32_32x32x16_f16 v[0:15], a[148:151], v[168:171], v[0:15]
	ds_read_b128 v[168:171], v193 offset:18432
	v_exp_f32_e32 v202, v158
	v_add_f32_e32 v201, 1.0, v201
	v_mfma_f32_32x32x16_f16 v[16:31], a[148:151], v[172:175], v[16:31]
	ds_read_b128 v[172:175], v193 offset:19456
	global_load_lds_dwordx4 v192, s[44:45] offset:3072 sc1
	v_exp_f32_e32 v203, v159
	v_add_f32_e32 v202, 1.0, v202
	v_mfma_f32_32x32x16_f16 v[0:15], a[152:155], v[176:179], v[0:15]
	ds_read_b128 v[176:179], v193 offset:20480
	v_add_f32_e32 v203, 1.0, v203
	v_rcp_f32_e32 v200, v200
	v_mfma_f32_32x32x16_f16 v[16:31], a[152:155], v[180:183], v[16:31]
	ds_read_b128 v[180:183], v193 offset:21504
	v_rcp_f32_e32 v201, v201
	v_fma_f32 v200, v200, 2.0, -1.0
	s_waitcnt lgkmcnt(2)
	v_mfma_f32_32x32x16_f16 v[0:15], a[156:159], v[184:187], v[0:15]
	ds_read_b128 v[184:187], v193 offset:22528
	v_rcp_f32_e32 v202, v202
	v_fma_f32 v201, v201, 2.0, -1.0
	v_mul_f32_e32 v216, v212, v200
	v_mfma_f32_32x32x16_f16 v[16:31], a[156:159], v[188:191], v[16:31]
	ds_read_b128 v[188:191], v193 offset:23552
	s_mov_b32 m0, s53
	s_add_u32 s44, s34, 0x1000
	s_addc_u32 s45, s35, 0
	global_load_lds_dwordx4 v192, s[44:45] sc1
	v_rcp_f32_e32 v203, v203
	v_fma_f32 v202, v202, 2.0, -1.0
	v_mul_f32_e32 v217, v213, v201
	v_mfma_f32_32x32x16_f16 v[0:15], a[160:163], v[160:163], v[0:15]
	ds_read_b128 v[160:163], v193 offset:24576
	v_fma_f32 v203, v203, 2.0, -1.0
	v_mul_f32_e32 v218, v214, v202
	v_mfma_f32_32x32x16_f16 v[16:31], a[160:163], v[164:167], v[16:31]
	ds_read_b128 v[164:167], v193 offset:25600
	v_mul_f32_e32 v219, v215, v203
	v_mul_f32_e32 v236, v216, v228
	v_mfma_f32_32x32x16_f16 v[0:15], a[164:167], v[168:171], v[0:15]
	ds_read_b128 v[168:171], v193 offset:26624
	v_mul_f32_e32 v237, v216, v232
	v_fmac_f32_e32 v236, v217, v229
	v_mfma_f32_32x32x16_f16 v[16:31], a[164:167], v[172:175], v[16:31]
	ds_read_b128 v[172:175], v193 offset:27648
	global_load_lds_dwordx4 v192, s[44:45] offset:1024 sc1
	v_fmac_f32_e32 v237, v217, v233
	v_fmac_f32_e32 v236, v218, v230
	s_waitcnt lgkmcnt(2)
	v_mfma_f32_32x32x16_f16 v[0:15], a[168:171], v[176:179], v[0:15]
	ds_read_b128 v[176:179], v193 offset:28672
	v_fmac_f32_e32 v237, v218, v234
	v_fmac_f32_e32 v236, v219, v231
	v_mfma_f32_32x32x16_f16 v[16:31], a[168:171], v[180:183], v[16:31]
	ds_read_b128 v[180:183], v193 offset:29696
	v_fmac_f32_e32 v237, v219, v235
	v_mov_b32_e32 v238, v236
	v_mfma_f32_32x32x16_f16 v[0:15], a[172:175], v[184:187], v[0:15]
	ds_read_b128 v[184:187], v193 offset:30720
	v_mov_b32_e32 v240, v237
	v_cvt_pk_f16_f32 v222, v216, v217
	v_mfma_f32_32x32x16_f16 v[16:31], a[172:175], v[188:191], v[16:31]
	ds_read_b128 v[188:191], v193 offset:31744
	global_load_lds_dwordx4 v192, s[44:45] offset:2048 sc1
	v_permlane32_swap_b32_e32 v236, v238
	v_permlane32_swap_b32_e32 v237, v240
	v_add_f32_e32 v238, v236, v238
	v_add_f32_e32 v239, v237, v240
	ds_write_b64 v248, v[238:239] offset:1792
	s_waitcnt vmcnt(7)
	s_barrier
	v_mfma_f32_32x32x16_f16 v[0:15], a[176:179], v[160:163], v[0:15]
	ds_read_b128 v[160:163], v193 offset:32768
	v_cvt_pk_f16_f32 v223, v218, v219
	v_mfma_f32_32x32x16_f16 v[16:31], a[176:179], v[164:167], v[16:31]
	ds_read_b128 v[164:167], v193 offset:33792
	v_permlane32_swap_b32_e32 v220, v222
	v_permlane32_swap_b32_e32 v221, v223
	s_cmp_eq_u32 s31, 0
	s_cbranch_scc1 .LD_slow18
	global_store_dwordx4 v195, v[220:223], s[36:37] offset:0

.LD_join21:
	ds_read_b64 v[200:201], v249 offset:1536
	ds_read_b64 v[202:203], v249 offset:3584
	ds_read_b64 v[204:205], v249 offset:5632
	ds_read_b64 v[206:207], v249 offset:7680
	v_mfma_f32_32x32x16_f16 v[16:31], a[212:215], v[172:175], v[16:31]
	ds_read_b128 v[172:175], v193 offset:52224
	global_load_lds_dwordx4 v192, s[44:45] offset:3072 sc1
	s_waitcnt lgkmcnt(6)
	v_mfma_f32_32x32x16_f16 v[0:15], a[216:219], v[176:179], v[0:15]
	ds_read_b128 v[176:179], v193 offset:53248
	v_mfma_f32_32x32x16_f16 v[16:31], a[216:219], v[180:183], v[16:31]
	ds_read_b128 v[180:183], v193 offset:54272
	v_mfma_f32_32x32x16_f16 v[0:15], a[220:223], v[184:187], v[0:15]
	ds_read_b128 v[184:187], v193 offset:55296
	v_mfma_f32_32x32x16_f16 v[16:31], a[220:223], v[188:191], v[16:31]
	ds_read_b128 v[188:191], v193 offset:56320
	s_mov_b32 m0, s55
	s_add_u32 s44, s34, 0x9000
	s_addc_u32 s45, s35, 0
	global_load_lds_dwordx4 v192, s[44:45] sc1
	v_mfma_f32_32x32x16_f16 v[0:15], a[224:227], v[160:163], v[0:15]
	ds_read_b128 v[160:163], v193 offset:57344
	v_mfma_f32_32x32x16_f16 v[16:31], a[224:227], v[164:167], v[16:31]
	ds_read_b128 v[164:167], v193 offset:58368
	s_waitcnt lgkmcnt(2)
	v_mfma_f32_32x32x16_f16 v[0:15], a[228:231], v[168:171], v[0:15]
	ds_read_b128 v[168:171], v193 offset:59392
	v_mfma_f32_32x32x16_f16 v[16:31], a[228:231], v[172:175], v[16:31]
	ds_read_b128 v[172:175], v193 offset:60416
	global_load_lds_dwordx4 v192, s[44:45] offset:1024 sc1
	v_mfma_f32_32x32x16_f16 v[0:15], a[232:235], v[176:179], v[0:15]
	ds_read_b128 v[176:179], v193 offset:61440
	v_mfma_f32_32x32x16_f16 v[16:31], a[232:235], v[180:183], v[16:31]
	ds_read_b128 v[180:183], v193 offset:62464
	v_mfma_f32_32x32x16_f16 v[0:15], a[236:239], v[184:187], v[0:15]
	ds_read_b128 v[184:187], v193 offset:63488
	v_add_f32_e32 v200, v200, v202
	v_add_f32_e32 v201, v201, v203
	v_add_f32_e32 v200, v200, v204
	v_add_f32_e32 v201, v201, v205
	v_add_f32_e32 v200, v200, v206
	v_add_f32_e32 v201, v201, v207
	global_store_dwordx2 v250, v[200:201], s[72:73]
	v_mfma_f32_32x32x16_f16 v[16:31], a[236:239], v[188:191], v[16:31]
	ds_read_b128 v[188:191], v193 offset:64512
	global_load_lds_dwordx4 v192, s[44:45] offset:2048 sc1
	s_waitcnt vmcnt(9)
	s_barrier
	s_waitcnt lgkmcnt(2)
	v_mfma_f32_32x32x16_f16 v[0:15], a[240:243], v[160:163], v[0:15]
	ds_read_b128 v[160:163], v192 offset:0
	v_mfma_f32_32x32x16_f16 v[16:31], a[240:243], v[164:167], v[16:31]
	ds_read_b128 v[164:167], v192 offset:1024
	v_mfma_f32_32x32x16_f16 v[0:15], a[244:247], v[168:171], v[0:15]
	ds_read_b128 v[168:171], v192 offset:2048
	s_and_b32 s64, s33, 1
	s_lshl_b32 s64, s64, 22
	s_add_u32 s64, s64, s50
	s_add_u32 s36, s6, s64
	s_addc_u32 s37, s7, 0
	s_lshl_b32 s64, s33, 3
	s_add_u32 s64, s64, s29
	s_lshl_b32 s64, s64, 5
	s_add_u32 s64, s64, s30
	s_lshl_b32 s64, s64, 2
	s_add_u32 s40, s8, s64
	s_addc_u32 s41, s9, 0
	s_lshl_b32 s64, s33, 19
	s_add_u32 s72, s62, s64
	s_addc_u32 s73, s63, 0
	v_mfma_f32_32x32x16_f16 v[16:31], a[244:247], v[172:175], v[16:31]
	ds_read_b128 v[172:175], v192 offset:3072
	global_load_lds_dwordx4 v192, s[44:45] offset:3072 sc1
	v_mfma_f32_32x32x16_f16 v[0:15], a[248:251], v[176:179], v[0:15]
	ds_read_b128 v[176:179], v192 offset:4096
	v_mfma_f32_32x32x16_f16 v[16:31], a[248:251], v[180:183], v[16:31]
	ds_read_b128 v[180:183], v192 offset:5120
	s_waitcnt lgkmcnt(2)
	v_mfma_f32_32x32x16_f16 v[0:15], a[252:255], v[184:187], v[0:15]
	ds_read_b128 v[184:187], v192 offset:6144
	v_mfma_f32_32x32x16_f16 v[16:31], a[252:255], v[188:191], v[16:31]
	ds_read_b128 v[188:191], v192 offset:7168
	s_mov_b32 m0, s56
	s_add_u32 s44, s34, 0x10000
	s_addc_u32 s45, s35, 0
	global_load_lds_dwordx4 v192, s[44:45] sc1
	s_nop 3
	s_waitcnt lgkmcnt(2)
	v_mfma_f32_32x32x16_f16 v[32:47], a[0:3], v[160:163], v[32:47]
	ds_read_b128 v[160:163], v192 offset:8192
	v_exp_f32_e32 v200, v0
	v_mfma_f32_32x32x16_f16 v[48:63], a[0:3], v[164:167], v[48:63]
	ds_read_b128 v[164:167], v192 offset:9216
	s_lshl_b32 s64, s71, 3
	s_add_u32 s64, s64, s29
	s_lshl_b32 s64, s64, 7
	s_add_u32 s38, s8, s64
	s_addc_u32 s39, s9, 0
	global_load_dword v251, v196, s[38:39] sc1
	v_exp_f32_e32 v201, v1
	v_add_f32_e32 v200, 1.0, v200
	v_mfma_f32_32x32x16_f16 v[32:47], a[4:7], v[168:171], v[32:47]
	ds_read_b128 v[168:171], v192 offset:10240
	v_exp_f32_e32 v202, v2
	v_add_f32_e32 v201, 1.0, v201
	v_mfma_f32_32x32x16_f16 v[48:63], a[4:7], v[172:175], v[48:63]
	ds_read_b128 v[172:175], v192 offset:11264
	global_load_lds_dwordx4 v192, s[44:45] offset:1024 sc1
	v_exp_f32_e32 v203, v3
	v_add_f32_e32 v202, 1.0, v202
	v_mfma_f32_32x32x16_f16 v[32:47], a[8:11], v[176:179], v[32:47]
	ds_read_b128 v[176:179], v192 offset:12288
	v_exp_f32_e32 v204, v4
	v_add_f32_e32 v203, 1.0, v203
	v_mfma_f32_32x32x16_f16 v[48:63], a[8:11], v[180:183], v[48:63]
	ds_read_b128 v[180:183], v192 offset:13312
	v_exp_f32_e32 v205, v5
	v_add_f32_e32 v204, 1.0, v204
	s_waitcnt lgkmcnt(2)
	v_mfma_f32_32x32x16_f16 v[32:47], a[12:15], v[184:187], v[32:47]
	ds_read_b128 v[184:187], v192 offset:14336
	v_exp_f32_e32 v206, v6
	v_add_f32_e32 v205, 1.0, v205
	v_mfma_f32_32x32x16_f16 v[48:63], a[12:15], v[188:191], v[48:63]
	ds_read_b128 v[188:191], v192 offset:15360
	global_load_lds_dwordx4 v192, s[44:45] offset:2048 sc1
	v_exp_f32_e32 v207, v7
	v_add_f32_e32 v206, 1.0, v206
	v_mfma_f32_32x32x16_f16 v[32:47], a[16:19], v[160:163], v[32:47]
	ds_read_b128 v[160:163], v192 offset:16384
	v_exp_f32_e32 v208, v8
	v_add_f32_e32 v207, 1.0, v207
	v_mfma_f32_32x32x16_f16 v[48:63], a[16:19], v[164:167], v[48:63]
	ds_read_b128 v[164:167], v192 offset:17408
	v_exp_f32_e32 v209, v9
	v_add_f32_e32 v208, 1.0, v208
	v_mfma_f32_32x32x16_f16 v[32:47], a[20:23], v[168:171], v[32:47]
	ds_read_b128 v[168:171], v192 offset:18432
	v_exp_f32_e32 v210, v10
	v_add_f32_e32 v209, 1.0, v209
	v_mfma_f32_32x32x16_f16 v[48:63], a[20:23], v[172:175], v[48:63]
	ds_read_b128 v[172:175], v192 offset:19456
	global_load_lds_dwordx4 v192, s[44:45] offset:3072 sc1
	v_exp_f32_e32 v211, v11
	v_add_f32_e32 v210, 1.0, v210
	s_waitcnt lgkmcnt(2)
	v_mfma_f32_32x32x16_f16 v[32:47], a[24:27], v[176:179], v[32:47]
	ds_read_b128 v[176:179], v192 offset:20480
	v_exp_f32_e32 v212, v12
	v_add_f32_e32 v211, 1.0, v211
	v_mfma_f32_32x32x16_f16 v[48:63], a[24:27], v[180:183], v[48:63]
	ds_read_b128 v[180:183], v192 offset:21504
	v_exp_f32_e32 v213, v13
	v_add_f32_e32 v212, 1.0, v212
	v_mfma_f32_32x32x16_f16 v[32:47], a[28:31], v[184:187], v[32:47]
	ds_read_b128 v[184:187], v192 offset:22528
	v_exp_f32_e32 v214, v14
	v_add_f32_e32 v213, 1.0, v213
	v_mfma_f32_32x32x16_f16 v[48:63], a[28:31], v[188:191], v[48:63]
	ds_read_b128 v[188:191], v192 offset:23552
	s_mov_b32 m0, s57
	s_add_u32 s44, s34, 0x11000
	s_addc_u32 s45, s35, 0
	global_load_lds_dwordx4 v192, s[44:45] sc1
	v_exp_f32_e32 v215, v15
	v_add_f32_e32 v214, 1.0, v214
	v_mfma_f32_32x32x16_f16 v[32:47], a[32:35], v[160:163], v[32:47]
	ds_read_b128 v[160:163], v192 offset:24576
	v_add_f32_e32 v215, 1.0, v215
	v_rcp_f32_e32 v200, v200
	v_mfma_f32_32x32x16_f16 v[48:63], a[32:35], v[164:167], v[48:63]
	ds_read_b128 v[164:167], v192 offset:25600
	v_rcp_f32_e32 v201, v201
	s_waitcnt lgkmcnt(2)
	v_mfma_f32_32x32x16_f16 v[32:47], a[36:39], v[168:171], v[32:47]
	ds_read_b128 v[168:171], v192 offset:26624
	v_rcp_f32_e32 v202, v202
	v_mfma_f32_32x32x16_f16 v[48:63], a[36:39], v[172:175], v[48:63]
	ds_read_b128 v[172:175], v192 offset:27648
	global_load_lds_dwordx4 v192, s[44:45] offset:1024 sc1
	v_rcp_f32_e32 v203, v203
	v_mfma_f32_32x32x16_f16 v[32:47], a[40:43], v[176:179], v[32:47]
	ds_read_b128 v[176:179], v192 offset:28672
	v_rcp_f32_e32 v204, v204
	v_mfma_f32_32x32x16_f16 v[48:63], a[40:43], v[180:183], v[48:63]
	ds_read_b128 v[180:183], v192 offset:29696
	v_rcp_f32_e32 v205, v205
	v_mul_f32_e32 v204, v204, v128
	v_mfma_f32_32x32x16_f16 v[32:47], a[44:47], v[184:187], v[32:47]
	ds_read_b128 v[184:187], v192 offset:30720
	v_rcp_f32_e32 v206, v206
	v_mul_f32_e32 v205, v205, v129
	v_mfma_f32_32x32x16_f16 v[48:63], a[44:47], v[188:191], v[48:63]
	ds_read_b128 v[188:191], v192 offset:31744
	global_load_lds_dwordx4 v192, s[44:45] offset:2048 sc1
	v_rcp_f32_e32 v207, v207
	v_mul_f32_e32 v206, v206, v130
	s_waitcnt vmcnt(8)
	s_barrier
	s_waitcnt lgkmcnt(2)
	v_mfma_f32_32x32x16_f16 v[32:47], a[48:51], v[160:163], v[32:47]
	ds_read_b128 v[160:163], v192 offset:32768
	v_rcp_f32_e32 v208, v208
	v_mul_f32_e32 v207, v207, v131
	v_mfma_f32_32x32x16_f16 v[48:63], a[48:51], v[164:167], v[48:63]
	ds_read_b128 v[164:167], v192 offset:33792
	v_rcp_f32_e32 v209, v209
	v_fmamk_f32 v208, v208, 0xc0b8aa3b, v198
	v_mfma_f32_32x32x16_f16 v[32:47], a[52:55], v[168:171], v[32:47]
	ds_read_b128 v[168:171], v192 offset:34816
	v_rcp_f32_e32 v210, v210
	v_fmamk_f32 v209, v209, 0xc0b8aa3b, v198
	v_fma_f32 v128, v200, v208, v204
	v_mfma_f32_32x32x16_f16 v[48:63], a[52:55], v[172:175], v[48:63]
	ds_read_b128 v[172:175], v192 offset:35840
	global_load_lds_dwordx4 v192, s[44:45] offset:3072 sc1
	v_rcp_f32_e32 v211, v211
	v_fmamk_f32 v210, v210, 0xc0b8aa3b, v198
	v_fma_f32 v129, v201, v209, v205
	v_mfma_f32_32x32x16_f16 v[32:47], a[56:59], v[176:179], v[32:47]
	ds_read_b128 v[176:179], v192 offset:36864
	v_rcp_f32_e32 v212, v212
	v_fmamk_f32 v211, v211, 0xc0b8aa3b, v198
	v_fma_f32 v130, v202, v210, v206
	v_mfma_f32_32x32x16_f16 v[48:63], a[56:59], v[180:183], v[48:63]
	ds_read_b128 v[180:183], v192 offset:37888
	v_rcp_f32_e32 v213, v213
	v_fma_f32 v131, v203, v211, v207
	s_waitcnt lgkmcnt(2)
	v_mfma_f32_32x32x16_f16 v[32:47], a[60:63], v[184:187], v[32:47]
	ds_read_b128 v[184:187], v192 offset:38912
	v_rcp_f32_e32 v214, v214
	v_mfma_f32_32x32x16_f16 v[48:63], a[60:63], v[188:191], v[48:63]
	ds_read_b128 v[188:191], v192 offset:39936
	s_mov_b32 m0, s58
	s_add_u32 s44, s34, 0x18000
	s_addc_u32 s45, s35, 0
	global_load_lds_dwordx4 v192, s[44:45] sc1
	v_rcp_f32_e32 v215, v215
	v_mfma_f32_32x32x16_f16 v[32:47], a[64:67], v[160:163], v[32:47]
	ds_read_b128 v[160:163], v192 offset:40960
	v_exp_f32_e32 v200, v128
	v_mfma_f32_32x32x16_f16 v[48:63], a[64:67], v[164:167], v[48:63]
	ds_read_b128 v[164:167], v192 offset:41984
	v_exp_f32_e32 v201, v129
	v_add_f32_e32 v200, 1.0, v200
	v_mfma_f32_32x32x16_f16 v[32:47], a[68:71], v[168:171], v[32:47]
	ds_read_b128 v[168:171], v192 offset:43008
	v_exp_f32_e32 v202, v130
	v_add_f32_e32 v201, 1.0, v201
	v_mfma_f32_32x32x16_f16 v[48:63], a[68:71], v[172:175], v[48:63]
	ds_read_b128 v[172:175], v192 offset:44032
	global_load_lds_dwordx4 v192, s[44:45] offset:1024 sc1
	v_exp_f32_e32 v203, v131
	v_add_f32_e32 v202, 1.0, v202
	s_waitcnt lgkmcnt(2)
	v_mfma_f32_32x32x16_f16 v[32:47], a[72:75], v[176:179], v[32:47]
	ds_read_b128 v[176:179], v192 offset:45056
	v_add_f32_e32 v203, 1.0, v203
	v_rcp_f32_e32 v200, v200
	v_mfma_f32_32x32x16_f16 v[48:63], a[72:75], v[180:183], v[48:63]
	ds_read_b128 v[180:183], v192 offset:46080
	v_rcp_f32_e32 v201, v201
	v_fma_f32 v200, v200, 2.0, -1.0
	v_mfma_f32_32x32x16_f16 v[32:47], a[76:79], v[184:187], v[32:47]
	ds_read_b128 v[184:187], v192 offset:47104
	v_rcp_f32_e32 v202, v202
	v_fma_f32 v201, v201, 2.0, -1.0
	v_mul_f32_e32 v216, v212, v200
	v_mfma_f32_32x32x16_f16 v[48:63], a[76:79], v[188:191], v[48:63]
	ds_read_b128 v[188:191], v192 offset:48128
	global_load_lds_dwordx4 v192, s[44:45] offset:2048 sc1
	v_rcp_f32_e32 v203, v203
	v_fma_f32 v202, v202, 2.0, -1.0
	v_mul_f32_e32 v217, v213, v201
	v_mfma_f32_32x32x16_f16 v[32:47], a[80:83], v[160:163], v[32:47]
	ds_read_b128 v[160:163], v192 offset:49152
	v_fma_f32 v203, v203, 2.0, -1.0
	v_mul_f32_e32 v218, v214, v202
	v_exp_f32_e32 v200, v16
	v_mfma_f32_32x32x16_f16 v[48:63], a[80:83], v[164:167], v[48:63]
	ds_read_b128 v[164:167], v192 offset:50176
	v_mul_f32_e32 v219, v215, v203
	v_mul_f32_e32 v236, v216, v228
	v_exp_f32_e32 v201, v17
	s_waitcnt lgkmcnt(2)
	v_mfma_f32_32x32x16_f16 v[32:47], a[84:87], v[168:171], v[32:47]
	ds_read_b128 v[168:171], v192 offset:51200
	v_mul_f32_e32 v237, v216, v232
	v_fmac_f32_e32 v236, v217, v229
	v_exp_f32_e32 v202, v18
	v_mfma_f32_32x32x16_f16 v[48:63], a[84:87], v[172:175], v[48:63]
	ds_read_b128 v[172:175], v192 offset:52224
	global_load_lds_dwordx4 v192, s[44:45] offset:3072 sc1
	v_fmac_f32_e32 v237, v217, v233
	v_fmac_f32_e32 v236, v218, v230
	v_exp_f32_e32 v203, v19
	v_mfma_f32_32x32x16_f16 v[32:47], a[88:91], v[176:179], v[32:47]
	ds_read_b128 v[176:179], v192 offset:53248
	v_fmac_f32_e32 v237, v218, v234
	v_fmac_f32_e32 v236, v219, v231
	v_exp_f32_e32 v204, v20
	v_mfma_f32_32x32x16_f16 v[48:63], a[88:91], v[180:183], v[48:63]
	ds_read_b128 v[180:183], v192 offset:54272
	v_fmac_f32_e32 v237, v219, v235
	v_mov_b32_e32 v238, v236
	v_exp_f32_e32 v205, v21
	v_mfma_f32_32x32x16_f16 v[32:47], a[92:95], v[184:187], v[32:47]
	ds_read_b128 v[184:187], v192 offset:55296
	v_mov_b32_e32 v240, v237
	v_cvt_pk_f16_f32 v220, v216, v217
	v_exp_f32_e32 v206, v22
	v_mfma_f32_32x32x16_f16 v[48:63], a[92:95], v[188:191], v[48:63]
	ds_read_b128 v[188:191], v192 offset:56320
	s_mov_b32 m0, s59
	s_add_u32 s44, s34, 0x19000
	s_addc_u32 s45, s35, 0
	global_load_lds_dwordx4 v192, s[44:45] sc1
	v_permlane32_swap_b32_e32 v236, v238
	v_permlane32_swap_b32_e32 v237, v240
	v_add_f32_e32 v238, v236, v238
	v_add_f32_e32 v239, v237, v240
	ds_write_b64 v248, v[238:239] offset:0
	v_exp_f32_e32 v207, v23
	s_waitcnt lgkmcnt(3)
	v_mfma_f32_32x32x16_f16 v[32:47], a[96:99], v[160:163], v[32:47]
	ds_read_b128 v[160:163], v192 offset:57344
	v_cvt_pk_f16_f32 v221, v218, v219
	v_exp_f32_e32 v208, v24
	v_add_f32_e32 v200, 1.0, v200
	v_mfma_f32_32x32x16_f16 v[48:63], a[96:99], v[164:167], v[48:63]
	ds_read_b128 v[164:167], v192 offset:58368
	v_exp_f32_e32 v209, v25
	v_add_f32_e32 v201, 1.0, v201
	v_add_f32_e32 v202, 1.0, v202
	v_mfma_f32_32x32x16_f16 v[32:47], a[100:103], v[168:171], v[32:47]
	ds_read_b128 v[168:171], v192 offset:59392
	v_exp_f32_e32 v210, v26
	v_add_f32_e32 v203, 1.0, v203
	v_add_f32_e32 v204, 1.0, v204
	v_mfma_f32_32x32x16_f16 v[48:63], a[100:103], v[172:175], v[48:63]
	ds_read_b128 v[172:175], v192 offset:60416
	global_load_lds_dwordx4 v192, s[44:45] offset:1024 sc1
	v_exp_f32_e32 v211, v27
	v_add_f32_e32 v205, 1.0, v205
	v_add_f32_e32 v206, 1.0, v206
	v_mfma_f32_32x32x16_f16 v[32:47], a[104:107], v[176:179], v[32:47]
	ds_read_b128 v[176:179], v192 offset:61440
	v_exp_f32_e32 v212, v28
	v_add_f32_e32 v207, 1.0, v207
	v_add_f32_e32 v208, 1.0, v208
	v_mfma_f32_32x32x16_f16 v[48:63], a[104:107], v[180:183], v[48:63]
	ds_read_b128 v[180:183], v192 offset:62464
	v_exp_f32_e32 v213, v29
	v_add_f32_e32 v209, 1.0, v209
	v_add_f32_e32 v210, 1.0, v210
	s_waitcnt lgkmcnt(2)
	v_mfma_f32_32x32x16_f16 v[32:47], a[108:111], v[184:187], v[32:47]
	ds_read_b128 v[184:187], v192 offset:63488
	v_exp_f32_e32 v214, v30
	v_add_f32_e32 v211, 1.0, v211
	v_add_f32_e32 v212, 1.0, v212
	s_add_u32 s46, s42, 0x6000
	s_addc_u32 s47, s43, 0
	global_load_dwordx4 v[96:99], v192, s[46:47] offset:0
	v_mfma_f32_32x32x16_f16 v[48:63], a[108:111], v[188:191], v[48:63]
	ds_read_b128 v[188:191], v192 offset:64512
	global_load_lds_dwordx4 v192, s[44:45] offset:2048 sc1
	v_exp_f32_e32 v215, v31
	v_add_f32_e32 v213, 1.0, v213
	v_add_f32_e32 v214, 1.0, v214
	global_load_dwordx4 v[100:103], v192, s[46:47] offset:1024
	global_load_dwordx4 v[104:107], v192, s[46:47] offset:2048
	s_waitcnt vmcnt(10)
	s_barrier
	v_mfma_f32_32x32x16_f16 v[32:47], a[112:115], v[160:163], v[32:47]
	ds_read_b128 v[160:163], v193 offset:0
	v_add_f32_e32 v215, 1.0, v215
	v_rcp_f32_e32 v200, v200
	global_load_dwordx4 v[108:111], v192, s[46:47] offset:3072
	s_add_u32 s46, s42, 0x7000
	s_addc_u32 s47, s43, 0
	v_mfma_f32_32x32x16_f16 v[48:63], a[112:115], v[164:167], v[48:63]
	ds_read_b128 v[164:167], v193 offset:1024
	v_rcp_f32_e32 v201, v201
	global_load_dwordx4 v[112:115], v192, s[46:47] offset:0
	global_load_dwordx4 v[116:119], v192, s[46:47] offset:1024
	v_mfma_f32_32x32x16_f16 v[32:47], a[116:119], v[168:171], v[32:47]
	ds_read_b128 v[168:171], v193 offset:2048
	v_rcp_f32_e32 v202, v202
	global_load_dwordx4 v[120:123], v192, s[46:47] offset:2048
	global_load_dwordx4 v[124:127], v192, s[46:47] offset:3072
	v_mfma_f32_32x32x16_f16 v[48:63], a[116:119], v[172:175], v[48:63]
	ds_read_b128 v[172:175], v193 offset:3072
	global_load_lds_dwordx4 v192, s[44:45] offset:3072 sc1
	v_rcp_f32_e32 v203, v203
	s_waitcnt lgkmcnt(2)
	v_mfma_f32_32x32x16_f16 v[32:47], a[120:123], v[176:179], v[32:47]
	ds_read_b128 v[176:179], v193 offset:4096
	v_rcp_f32_e32 v204, v204
	v_mfma_f32_32x32x16_f16 v[48:63], a[120:123], v[180:183], v[48:63]
	ds_read_b128 v[180:183], v193 offset:5120
	v_rcp_f32_e32 v205, v205
	v_mul_f32_e32 v204, v204, v132
	v_mfma_f32_32x32x16_f16 v[32:47], a[124:127], v[184:187], v[32:47]
	ds_read_b128 v[184:187], v193 offset:6144
	v_rcp_f32_e32 v206, v206
	v_mul_f32_e32 v205, v205, v133
	v_mfma_f32_32x32x16_f16 v[48:63], a[124:127], v[188:191], v[48:63]
	ds_read_b128 v[188:191], v193 offset:7168
	v_cmp_gt_u32_e32 vcc, 3, v251
	s_cbranch_vccnz .LD_tpoll23
.LD_tok22:
	s_and_b32 s64, s71, 1
	s_lshl_b32 s64, s64, 22
	s_add_u32 s64, s64, s49
	s_add_u32 s64, s64, 0x40000
	s_add_u32 s34, s6, s64
	s_addc_u32 s35, s7, 0
	s_mov_b32 m0, s52
	s_add_u32 s44, s34, 0x0
	s_addc_u32 s45, s35, 0
	global_load_lds_dwordx4 v192, s[44:45] sc1
	v_rcp_f32_e32 v207, v207
	v_mul_f32_e32 v206, v206, v134
	v_mfma_f32_32x32x16_f16 v[32:47], a[128:131], v[160:163], v[32:47]
	ds_read_b128 v[160:163], v193 offset:8192
	v_rcp_f32_e32 v208, v208
	v_mul_f32_e32 v207, v207, v135
	v_mfma_f32_32x32x16_f16 v[48:63], a[128:131], v[164:167], v[48:63]
	ds_read_b128 v[164:167], v193 offset:9216
	v_rcp_f32_e32 v209, v209
	v_fmamk_f32 v208, v208, 0xc0b8aa3b, v198
	s_waitcnt lgkmcnt(2)
	v_mfma_f32_32x32x16_f16 v[32:47], a[132:135], v[168:171], v[32:47]
	ds_read_b128 v[168:171], v193 offset:10240
	v_rcp_f32_e32 v210, v210
	v_fmamk_f32 v209, v209, 0xc0b8aa3b, v198
	v_fma_f32 v132, v200, v208, v204
	v_mfma_f32_32x32x16_f16 v[48:63], a[132:135], v[172:175], v[48:63]
	ds_read_b128 v[172:175], v193 offset:11264
	global_load_lds_dwordx4 v192, s[44:45] offset:1024 sc1
	v_rcp_f32_e32 v211, v211
	v_fmamk_f32 v210, v210, 0xc0b8aa3b, v198
	v_fma_f32 v133, v201, v209, v205
	v_mfma_f32_32x32x16_f16 v[32:47], a[136:139], v[176:179], v[32:47]
	ds_read_b128 v[176:179], v193 offset:12288
	v_rcp_f32_e32 v212, v212
	v_fmamk_f32 v211, v211, 0xc0b8aa3b, v198
	v_fma_f32 v134, v202, v210, v206
	v_mfma_f32_32x32x16_f16 v[48:63], a[136:139], v[180:183], v[48:63]
	ds_read_b128 v[180:183], v193 offset:13312
	v_rcp_f32_e32 v213, v213
	v_fma_f32 v135, v203, v211, v207
	v_mfma_f32_32x32x16_f16 v[32:47], a[140:143], v[184:187], v[32:47]
	ds_read_b128 v[184:187], v193 offset:14336
	v_rcp_f32_e32 v214, v214
	v_mfma_f32_32x32x16_f16 v[48:63], a[140:143], v[188:191], v[48:63]
	ds_read_b128 v[188:191], v193 offset:15360
	global_load_lds_dwordx4 v192, s[44:45] offset:2048 sc1
	v_rcp_f32_e32 v215, v215
	s_waitcnt lgkmcnt(2)
	v_mfma_f32_32x32x16_f16 v[32:47], a[144:147], v[160:163], v[32:47]
	ds_read_b128 v[160:163], v193 offset:16384
	v_exp_f32_e32 v200, v132
	v_mfma_f32_32x32x16_f16 v[48:63], a[144:147], v[164:167], v[48:63]
	ds_read_b128 v[164:167], v193 offset:17408
	v_exp_f32_e32 v201, v133
	v_add_f32_e32 v200, 1.0, v200
	v_mfma_f32_32x32x16_f16 v[32:47], a[148:151], v[168:171], v[32:47]
	ds_read_b128 v[168:171], v193 offset:18432
	v_exp_f32_e32 v202, v134
	v_add_f32_e32 v201, 1.0, v201
	v_mfma_f32_32x32x16_f16 v[48:63], a[148:151], v[172:175], v[48:63]
	ds_read_b128 v[172:175], v193 offset:19456
	global_load_lds_dwordx4 v192, s[44:45] offset:3072 sc1
	v_exp_f32_e32 v203, v135
	v_add_f32_e32 v202, 1.0, v202
	v_mfma_f32_32x32x16_f16 v[32:47], a[152:155], v[176:179], v[32:47]
	ds_read_b128 v[176:179], v193 offset:20480
	v_add_f32_e32 v203, 1.0, v203
	v_rcp_f32_e32 v200, v200
	v_mfma_f32_32x32x16_f16 v[48:63], a[152:155], v[180:183], v[48:63]
	ds_read_b128 v[180:183], v193 offset:21504
	v_rcp_f32_e32 v201, v201
	v_fma_f32 v200, v200, 2.0, -1.0
	s_waitcnt lgkmcnt(2)
	v_mfma_f32_32x32x16_f16 v[32:47], a[156:159], v[184:187], v[32:47]
	ds_read_b128 v[184:187], v193 offset:22528
	v_rcp_f32_e32 v202, v202
	v_fma_f32 v201, v201, 2.0, -1.0
	v_mul_f32_e32 v216, v212, v200
	v_mfma_f32_32x32x16_f16 v[48:63], a[156:159], v[188:191], v[48:63]
	ds_read_b128 v[188:191], v193 offset:23552
	s_mov_b32 m0, s53
	s_add_u32 s44, s34, 0x1000
	s_addc_u32 s45, s35, 0
	global_load_lds_dwordx4 v192, s[44:45] sc1
	v_rcp_f32_e32 v203, v203
	v_fma_f32 v202, v202, 2.0, -1.0
	v_mul_f32_e32 v217, v213, v201
	v_mfma_f32_32x32x16_f16 v[32:47], a[160:163], v[160:163], v[32:47]
	ds_read_b128 v[160:163], v193 offset:24576
	v_fma_f32 v203, v203, 2.0, -1.0
	v_mul_f32_e32 v218, v214, v202
	v_mfma_f32_32x32x16_f16 v[48:63], a[160:163], v[164:167], v[48:63]
	ds_read_b128 v[164:167], v193 offset:25600
	v_mul_f32_e32 v219, v215, v203
	v_mul_f32_e32 v236, v216, v228
	v_mfma_f32_32x32x16_f16 v[32:47], a[164:167], v[168:171], v[32:47]
	ds_read_b128 v[168:171], v193 offset:26624
	v_mul_f32_e32 v237, v216, v232
	v_fmac_f32_e32 v236, v217, v229
	v_mfma_f32_32x32x16_f16 v[48:63], a[164:167], v[172:175], v[48:63]
	ds_read_b128 v[172:175], v193 offset:27648
	global_load_lds_dwordx4 v192, s[44:45] offset:1024 sc1
	v_fmac_f32_e32 v237, v217, v233
	v_fmac_f32_e32 v236, v218, v230
	s_waitcnt lgkmcnt(2)
	v_mfma_f32_32x32x16_f16 v[32:47], a[168:171], v[176:179], v[32:47]
	ds_read_b128 v[176:179], v193 offset:28672
	v_fmac_f32_e32 v237, v218, v234
	v_fmac_f32_e32 v236, v219, v231
	v_mfma_f32_32x32x16_f16 v[48:63], a[168:171], v[180:183], v[48:63]
	ds_read_b128 v[180:183], v193 offset:29696
	v_fmac_f32_e32 v237, v219, v235
	v_mov_b32_e32 v238, v236
	v_mfma_f32_32x32x16_f16 v[32:47], a[172:175], v[184:187], v[32:47]
	ds_read_b128 v[184:187], v193 offset:30720
	v_mov_b32_e32 v240, v237
	v_cvt_pk_f16_f32 v222, v216, v217
	v_mfma_f32_32x32x16_f16 v[48:63], a[172:175], v[188:191], v[48:63]
	ds_read_b128 v[188:191], v193 offset:31744
	global_load_lds_dwordx4 v192, s[44:45] offset:2048 sc1
	v_permlane32_swap_b32_e32 v236, v238
	v_permlane32_swap_b32_e32 v237, v240
	v_add_f32_e32 v238, v236, v238
	v_add_f32_e32 v239, v237, v240
	ds_write_b64 v248, v[238:239] offset:256
	s_waitcnt vmcnt(7)
	s_barrier
	v_mfma_f32_32x32x16_f16 v[32:47], a[176:179], v[160:163], v[32:47]
	ds_read_b128 v[160:163], v193 offset:32768
	v_cvt_pk_f16_f32 v223, v218, v219
	v_mfma_f32_32x32x16_f16 v[48:63], a[176:179], v[164:167], v[48:63]
	ds_read_b128 v[164:167], v193 offset:33792
	v_permlane32_swap_b32_e32 v220, v222
	v_permlane32_swap_b32_e32 v221, v223
	s_cmp_eq_u32 s31, 0
	s_cbranch_scc1 .LD_slow24
	global_store_dwordx4 v195, v[220:223], s[36:37] offset:0

.LD_join27:
	ds_read_b64 v[200:201], v249 offset:0
	ds_read_b64 v[202:203], v249 offset:2048
	ds_read_b64 v[204:205], v249 offset:4096
	ds_read_b64 v[206:207], v249 offset:6144
	v_mfma_f32_32x32x16_f16 v[48:63], a[212:215], v[172:175], v[48:63]
	ds_read_b128 v[172:175], v193 offset:52224
	global_load_lds_dwordx4 v192, s[44:45] offset:3072 sc1
	s_waitcnt lgkmcnt(6)
	v_mfma_f32_32x32x16_f16 v[32:47], a[216:219], v[176:179], v[32:47]
	ds_read_b128 v[176:179], v193 offset:53248
	v_mfma_f32_32x32x16_f16 v[48:63], a[216:219], v[180:183], v[48:63]
	ds_read_b128 v[180:183], v193 offset:54272
	v_mfma_f32_32x32x16_f16 v[32:47], a[220:223], v[184:187], v[32:47]
	ds_read_b128 v[184:187], v193 offset:55296
	v_mfma_f32_32x32x16_f16 v[48:63], a[220:223], v[188:191], v[48:63]
	ds_read_b128 v[188:191], v193 offset:56320
	s_mov_b32 m0, s55
	s_add_u32 s44, s34, 0x9000
	s_addc_u32 s45, s35, 0
	global_load_lds_dwordx4 v192, s[44:45] sc1
	v_mfma_f32_32x32x16_f16 v[32:47], a[224:227], v[160:163], v[32:47]
	ds_read_b128 v[160:163], v193 offset:57344
	v_mfma_f32_32x32x16_f16 v[48:63], a[224:227], v[164:167], v[48:63]
	ds_read_b128 v[164:167], v193 offset:58368
	s_waitcnt lgkmcnt(2)
	v_mfma_f32_32x32x16_f16 v[32:47], a[228:231], v[168:171], v[32:47]
	ds_read_b128 v[168:171], v193 offset:59392
	v_mfma_f32_32x32x16_f16 v[48:63], a[228:231], v[172:175], v[48:63]
	ds_read_b128 v[172:175], v193 offset:60416
	global_load_lds_dwordx4 v192, s[44:45] offset:1024 sc1
	v_mfma_f32_32x32x16_f16 v[32:47], a[232:235], v[176:179], v[32:47]
	ds_read_b128 v[176:179], v193 offset:61440
	v_mfma_f32_32x32x16_f16 v[48:63], a[232:235], v[180:183], v[48:63]
	ds_read_b128 v[180:183], v193 offset:62464
	v_mfma_f32_32x32x16_f16 v[32:47], a[236:239], v[184:187], v[32:47]
	ds_read_b128 v[184:187], v193 offset:63488
	v_add_f32_e32 v200, v200, v202
	v_add_f32_e32 v201, v201, v203
	v_add_f32_e32 v200, v200, v204
	v_add_f32_e32 v201, v201, v205
	v_add_f32_e32 v200, v200, v206
	v_add_f32_e32 v201, v201, v207
	global_store_dwordx2 v250, v[200:201], s[72:73]
	v_mfma_f32_32x32x16_f16 v[48:63], a[236:239], v[188:191], v[48:63]
	ds_read_b128 v[188:191], v193 offset:64512
	global_load_lds_dwordx4 v192, s[44:45] offset:2048 sc1
	s_waitcnt vmcnt(9)
	s_barrier
	s_waitcnt lgkmcnt(2)
	v_mfma_f32_32x32x16_f16 v[32:47], a[240:243], v[160:163], v[32:47]
	ds_read_b128 v[160:163], v192 offset:0
	v_mfma_f32_32x32x16_f16 v[48:63], a[240:243], v[164:167], v[48:63]
	ds_read_b128 v[164:167], v192 offset:1024
	v_mfma_f32_32x32x16_f16 v[32:47], a[244:247], v[168:171], v[32:47]
	ds_read_b128 v[168:171], v192 offset:2048
	s_and_b32 s64, s33, 1
	s_lshl_b32 s64, s64, 22
	s_add_u32 s64, s64, s50
	s_add_u32 s64, s64, 0x20000
	s_add_u32 s36, s6, s64
	s_addc_u32 s37, s7, 0
	s_lshl_b32 s64, s33, 3
	s_add_u32 s64, s64, s29
	s_lshl_b32 s64, s64, 5
	s_add_u32 s64, s64, s30
	s_lshl_b32 s64, s64, 2
	s_add_u32 s40, s8, s64
	s_addc_u32 s41, s9, 0
	s_lshl_b32 s64, s33, 19
	s_add_u32 s64, s64, 0x200
	s_add_u32 s72, s62, s64
	s_addc_u32 s73, s63, 0
	v_mfma_f32_32x32x16_f16 v[48:63], a[244:247], v[172:175], v[48:63]
	ds_read_b128 v[172:175], v192 offset:3072
	global_load_lds_dwordx4 v192, s[44:45] offset:3072 sc1
	v_mfma_f32_32x32x16_f16 v[32:47], a[248:251], v[176:179], v[32:47]
	ds_read_b128 v[176:179], v192 offset:4096
	v_mfma_f32_32x32x16_f16 v[48:63], a[248:251], v[180:183], v[48:63]
	ds_read_b128 v[180:183], v192 offset:5120
	s_waitcnt lgkmcnt(2)
	v_mfma_f32_32x32x16_f16 v[32:47], a[252:255], v[184:187], v[32:47]
	ds_read_b128 v[184:187], v192 offset:6144
	v_mfma_f32_32x32x16_f16 v[48:63], a[252:255], v[188:191], v[48:63]
	ds_read_b128 v[188:191], v192 offset:7168
	s_mov_b32 m0, s56
	s_add_u32 s44, s34, 0x10000
	s_addc_u32 s45, s35, 0
	global_load_lds_dwordx4 v192, s[44:45] sc1
	s_nop 3
	s_waitcnt lgkmcnt(2)
	v_mfma_f32_32x32x16_f16 v[64:79], a[0:3], v[160:163], v[64:79]
	ds_read_b128 v[160:163], v192 offset:8192
	v_exp_f32_e32 v200, v32
	v_mfma_f32_32x32x16_f16 v[80:95], a[0:3], v[164:167], v[80:95]
	ds_read_b128 v[164:167], v192 offset:9216
	s_lshl_b32 s64, s71, 3
	s_add_u32 s64, s64, s29
	s_lshl_b32 s64, s64, 7
	s_add_u32 s38, s8, s64
	s_addc_u32 s39, s9, 0
	global_load_dword v251, v196, s[38:39] sc1
	v_exp_f32_e32 v201, v33
	v_add_f32_e32 v200, 1.0, v200
	v_mfma_f32_32x32x16_f16 v[64:79], a[4:7], v[168:171], v[64:79]
	ds_read_b128 v[168:171], v192 offset:10240
	v_exp_f32_e32 v202, v34
	v_add_f32_e32 v201, 1.0, v201
	v_mfma_f32_32x32x16_f16 v[80:95], a[4:7], v[172:175], v[80:95]
	ds_read_b128 v[172:175], v192 offset:11264
	global_load_lds_dwordx4 v192, s[44:45] offset:1024 sc1
	v_exp_f32_e32 v203, v35
	v_add_f32_e32 v202, 1.0, v202
	v_mfma_f32_32x32x16_f16 v[64:79], a[8:11], v[176:179], v[64:79]
	ds_read_b128 v[176:179], v192 offset:12288
	v_exp_f32_e32 v204, v36
	v_add_f32_e32 v203, 1.0, v203
	v_mfma_f32_32x32x16_f16 v[80:95], a[8:11], v[180:183], v[80:95]
	ds_read_b128 v[180:183], v192 offset:13312
	v_exp_f32_e32 v205, v37
	v_add_f32_e32 v204, 1.0, v204
	s_waitcnt lgkmcnt(2)
	v_mfma_f32_32x32x16_f16 v[64:79], a[12:15], v[184:187], v[64:79]
	ds_read_b128 v[184:187], v192 offset:14336
	v_exp_f32_e32 v206, v38
	v_add_f32_e32 v205, 1.0, v205
	v_mfma_f32_32x32x16_f16 v[80:95], a[12:15], v[188:191], v[80:95]
	ds_read_b128 v[188:191], v192 offset:15360
	global_load_lds_dwordx4 v192, s[44:45] offset:2048 sc1
	v_exp_f32_e32 v207, v39
	v_add_f32_e32 v206, 1.0, v206
	v_mfma_f32_32x32x16_f16 v[64:79], a[16:19], v[160:163], v[64:79]
	ds_read_b128 v[160:163], v192 offset:16384
	v_exp_f32_e32 v208, v40
	v_add_f32_e32 v207, 1.0, v207
	v_mfma_f32_32x32x16_f16 v[80:95], a[16:19], v[164:167], v[80:95]
	ds_read_b128 v[164:167], v192 offset:17408
	v_exp_f32_e32 v209, v41
	v_add_f32_e32 v208, 1.0, v208
	v_mfma_f32_32x32x16_f16 v[64:79], a[20:23], v[168:171], v[64:79]
	ds_read_b128 v[168:171], v192 offset:18432
	v_exp_f32_e32 v210, v42
	v_add_f32_e32 v209, 1.0, v209
	v_mfma_f32_32x32x16_f16 v[80:95], a[20:23], v[172:175], v[80:95]
	ds_read_b128 v[172:175], v192 offset:19456
	global_load_lds_dwordx4 v192, s[44:45] offset:3072 sc1
	v_exp_f32_e32 v211, v43
	v_add_f32_e32 v210, 1.0, v210
	s_waitcnt lgkmcnt(2)
	v_mfma_f32_32x32x16_f16 v[64:79], a[24:27], v[176:179], v[64:79]
	ds_read_b128 v[176:179], v192 offset:20480
	v_exp_f32_e32 v212, v44
	v_add_f32_e32 v211, 1.0, v211
	v_mfma_f32_32x32x16_f16 v[80:95], a[24:27], v[180:183], v[80:95]
	ds_read_b128 v[180:183], v192 offset:21504
	v_exp_f32_e32 v213, v45
	v_add_f32_e32 v212, 1.0, v212
	v_mfma_f32_32x32x16_f16 v[64:79], a[28:31], v[184:187], v[64:79]
	ds_read_b128 v[184:187], v192 offset:22528
	v_exp_f32_e32 v214, v46
	v_add_f32_e32 v213, 1.0, v213
	v_mfma_f32_32x32x16_f16 v[80:95], a[28:31], v[188:191], v[80:95]
	ds_read_b128 v[188:191], v192 offset:23552
	s_mov_b32 m0, s57
	s_add_u32 s44, s34, 0x11000
	s_addc_u32 s45, s35, 0
	global_load_lds_dwordx4 v192, s[44:45] sc1
	v_exp_f32_e32 v215, v47
	v_add_f32_e32 v214, 1.0, v214
	v_mfma_f32_32x32x16_f16 v[64:79], a[32:35], v[160:163], v[64:79]
	ds_read_b128 v[160:163], v192 offset:24576
	v_add_f32_e32 v215, 1.0, v215
	v_rcp_f32_e32 v200, v200
	v_mfma_f32_32x32x16_f16 v[80:95], a[32:35], v[164:167], v[80:95]
	ds_read_b128 v[164:167], v192 offset:25600
	v_rcp_f32_e32 v201, v201
	s_waitcnt lgkmcnt(2)
	v_mfma_f32_32x32x16_f16 v[64:79], a[36:39], v[168:171], v[64:79]
	ds_read_b128 v[168:171], v192 offset:26624
	v_rcp_f32_e32 v202, v202
	v_mfma_f32_32x32x16_f16 v[80:95], a[36:39], v[172:175], v[80:95]
	ds_read_b128 v[172:175], v192 offset:27648
	global_load_lds_dwordx4 v192, s[44:45] offset:1024 sc1
	v_rcp_f32_e32 v203, v203
	v_mfma_f32_32x32x16_f16 v[64:79], a[40:43], v[176:179], v[64:79]
	ds_read_b128 v[176:179], v192 offset:28672
	v_rcp_f32_e32 v204, v204
	v_mfma_f32_32x32x16_f16 v[80:95], a[40:43], v[180:183], v[80:95]
	ds_read_b128 v[180:183], v192 offset:29696
	v_rcp_f32_e32 v205, v205
	v_mul_f32_e32 v204, v204, v136
	v_mfma_f32_32x32x16_f16 v[64:79], a[44:47], v[184:187], v[64:79]
	ds_read_b128 v[184:187], v192 offset:30720
	v_rcp_f32_e32 v206, v206
	v_mul_f32_e32 v205, v205, v137
	v_mfma_f32_32x32x16_f16 v[80:95], a[44:47], v[188:191], v[80:95]
	ds_read_b128 v[188:191], v192 offset:31744
	global_load_lds_dwordx4 v192, s[44:45] offset:2048 sc1
	v_rcp_f32_e32 v207, v207
	v_mul_f32_e32 v206, v206, v138
	s_waitcnt vmcnt(8)
	s_barrier
	s_waitcnt lgkmcnt(2)
	v_mfma_f32_32x32x16_f16 v[64:79], a[48:51], v[160:163], v[64:79]
	ds_read_b128 v[160:163], v192 offset:32768
	v_rcp_f32_e32 v208, v208
	v_mul_f32_e32 v207, v207, v139
	v_mfma_f32_32x32x16_f16 v[80:95], a[48:51], v[164:167], v[80:95]
	ds_read_b128 v[164:167], v192 offset:33792
	v_rcp_f32_e32 v209, v209
	v_fmamk_f32 v208, v208, 0xc0b8aa3b, v198
	v_mfma_f32_32x32x16_f16 v[64:79], a[52:55], v[168:171], v[64:79]
	ds_read_b128 v[168:171], v192 offset:34816
	v_rcp_f32_e32 v210, v210
	v_fmamk_f32 v209, v209, 0xc0b8aa3b, v198
	v_fma_f32 v136, v200, v208, v204
	v_mfma_f32_32x32x16_f16 v[80:95], a[52:55], v[172:175], v[80:95]
	ds_read_b128 v[172:175], v192 offset:35840
	global_load_lds_dwordx4 v192, s[44:45] offset:3072 sc1
	v_rcp_f32_e32 v211, v211
	v_fmamk_f32 v210, v210, 0xc0b8aa3b, v198
	v_fma_f32 v137, v201, v209, v205
	v_mfma_f32_32x32x16_f16 v[64:79], a[56:59], v[176:179], v[64:79]
	ds_read_b128 v[176:179], v192 offset:36864
	v_rcp_f32_e32 v212, v212
	v_fmamk_f32 v211, v211, 0xc0b8aa3b, v198
	v_fma_f32 v138, v202, v210, v206
	v_mfma_f32_32x32x16_f16 v[80:95], a[56:59], v[180:183], v[80:95]
	ds_read_b128 v[180:183], v192 offset:37888
	v_rcp_f32_e32 v213, v213
	v_fma_f32 v139, v203, v211, v207
	s_waitcnt lgkmcnt(2)
	v_mfma_f32_32x32x16_f16 v[64:79], a[60:63], v[184:187], v[64:79]
	ds_read_b128 v[184:187], v192 offset:38912
	v_rcp_f32_e32 v214, v214
	v_mfma_f32_32x32x16_f16 v[80:95], a[60:63], v[188:191], v[80:95]
	ds_read_b128 v[188:191], v192 offset:39936
	s_mov_b32 m0, s58
	s_add_u32 s44, s34, 0x18000
	s_addc_u32 s45, s35, 0
	global_load_lds_dwordx4 v192, s[44:45] sc1
	v_rcp_f32_e32 v215, v215
	v_mfma_f32_32x32x16_f16 v[64:79], a[64:67], v[160:163], v[64:79]
	ds_read_b128 v[160:163], v192 offset:40960
	v_exp_f32_e32 v200, v136
	v_mfma_f32_32x32x16_f16 v[80:95], a[64:67], v[164:167], v[80:95]
	ds_read_b128 v[164:167], v192 offset:41984
	v_exp_f32_e32 v201, v137
	v_add_f32_e32 v200, 1.0, v200
	v_mfma_f32_32x32x16_f16 v[64:79], a[68:71], v[168:171], v[64:79]
	ds_read_b128 v[168:171], v192 offset:43008
	v_exp_f32_e32 v202, v138
	v_add_f32_e32 v201, 1.0, v201
	v_mfma_f32_32x32x16_f16 v[80:95], a[68:71], v[172:175], v[80:95]
	ds_read_b128 v[172:175], v192 offset:44032
	global_load_lds_dwordx4 v192, s[44:45] offset:1024 sc1
	v_exp_f32_e32 v203, v139
	v_add_f32_e32 v202, 1.0, v202
	s_waitcnt lgkmcnt(2)
	v_mfma_f32_32x32x16_f16 v[64:79], a[72:75], v[176:179], v[64:79]
	ds_read_b128 v[176:179], v192 offset:45056
	v_add_f32_e32 v203, 1.0, v203
	v_rcp_f32_e32 v200, v200
	v_mfma_f32_32x32x16_f16 v[80:95], a[72:75], v[180:183], v[80:95]
	ds_read_b128 v[180:183], v192 offset:46080
	v_rcp_f32_e32 v201, v201
	v_fma_f32 v200, v200, 2.0, -1.0
	v_mfma_f32_32x32x16_f16 v[64:79], a[76:79], v[184:187], v[64:79]
	ds_read_b128 v[184:187], v192 offset:47104
	v_rcp_f32_e32 v202, v202
	v_fma_f32 v201, v201, 2.0, -1.0
	v_mul_f32_e32 v216, v212, v200
	v_mfma_f32_32x32x16_f16 v[80:95], a[76:79], v[188:191], v[80:95]
	ds_read_b128 v[188:191], v192 offset:48128
	global_load_lds_dwordx4 v192, s[44:45] offset:2048 sc1
	v_rcp_f32_e32 v203, v203
	v_fma_f32 v202, v202, 2.0, -1.0
	v_mul_f32_e32 v217, v213, v201
	v_mfma_f32_32x32x16_f16 v[64:79], a[80:83], v[160:163], v[64:79]
	ds_read_b128 v[160:163], v192 offset:49152
	v_fma_f32 v203, v203, 2.0, -1.0
	v_mul_f32_e32 v218, v214, v202
	v_exp_f32_e32 v200, v48
	v_mfma_f32_32x32x16_f16 v[80:95], a[80:83], v[164:167], v[80:95]
	ds_read_b128 v[164:167], v192 offset:50176
	v_mul_f32_e32 v219, v215, v203
	v_mul_f32_e32 v236, v216, v228
	v_exp_f32_e32 v201, v49
	s_waitcnt lgkmcnt(2)
	v_mfma_f32_32x32x16_f16 v[64:79], a[84:87], v[168:171], v[64:79]
	ds_read_b128 v[168:171], v192 offset:51200
	v_mul_f32_e32 v237, v216, v232
	v_fmac_f32_e32 v236, v217, v229
	v_exp_f32_e32 v202, v50
	v_mfma_f32_32x32x16_f16 v[80:95], a[84:87], v[172:175], v[80:95]
	ds_read_b128 v[172:175], v192 offset:52224
	global_load_lds_dwordx4 v192, s[44:45] offset:3072 sc1
	v_fmac_f32_e32 v237, v217, v233
	v_fmac_f32_e32 v236, v218, v230
	v_exp_f32_e32 v203, v51
	v_mfma_f32_32x32x16_f16 v[64:79], a[88:91], v[176:179], v[64:79]
	ds_read_b128 v[176:179], v192 offset:53248
	v_fmac_f32_e32 v237, v218, v234
	v_fmac_f32_e32 v236, v219, v231
	v_exp_f32_e32 v204, v52
	v_mfma_f32_32x32x16_f16 v[80:95], a[88:91], v[180:183], v[80:95]
	ds_read_b128 v[180:183], v192 offset:54272
	v_fmac_f32_e32 v237, v219, v235
	v_mov_b32_e32 v238, v236
	v_exp_f32_e32 v205, v53
	v_mfma_f32_32x32x16_f16 v[64:79], a[92:95], v[184:187], v[64:79]
	ds_read_b128 v[184:187], v192 offset:55296
	v_mov_b32_e32 v240, v237
	v_cvt_pk_f16_f32 v220, v216, v217
	v_exp_f32_e32 v206, v54
	v_mfma_f32_32x32x16_f16 v[80:95], a[92:95], v[188:191], v[80:95]
	ds_read_b128 v[188:191], v192 offset:56320
	s_mov_b32 m0, s59
	s_add_u32 s44, s34, 0x19000
	s_addc_u32 s45, s35, 0
	global_load_lds_dwordx4 v192, s[44:45] sc1
	v_permlane32_swap_b32_e32 v236, v238
	v_permlane32_swap_b32_e32 v237, v240
	v_add_f32_e32 v238, v236, v238
	v_add_f32_e32 v239, v237, v240
	ds_write_b64 v248, v[238:239] offset:512
	v_exp_f32_e32 v207, v55
	s_waitcnt lgkmcnt(3)
	v_mfma_f32_32x32x16_f16 v[64:79], a[96:99], v[160:163], v[64:79]
	ds_read_b128 v[160:163], v192 offset:57344
	v_cvt_pk_f16_f32 v221, v218, v219
	v_exp_f32_e32 v208, v56
	v_add_f32_e32 v200, 1.0, v200
	v_mfma_f32_32x32x16_f16 v[80:95], a[96:99], v[164:167], v[80:95]
	ds_read_b128 v[164:167], v192 offset:58368
	v_exp_f32_e32 v209, v57
	v_add_f32_e32 v201, 1.0, v201
	v_add_f32_e32 v202, 1.0, v202
	v_mfma_f32_32x32x16_f16 v[64:79], a[100:103], v[168:171], v[64:79]
	ds_read_b128 v[168:171], v192 offset:59392
	v_exp_f32_e32 v210, v58
	v_add_f32_e32 v203, 1.0, v203
	v_add_f32_e32 v204, 1.0, v204
	v_mfma_f32_32x32x16_f16 v[80:95], a[100:103], v[172:175], v[80:95]
	ds_read_b128 v[172:175], v192 offset:60416
	global_load_lds_dwordx4 v192, s[44:45] offset:1024 sc1
	v_exp_f32_e32 v211, v59
	v_add_f32_e32 v205, 1.0, v205
	v_add_f32_e32 v206, 1.0, v206
	v_mfma_f32_32x32x16_f16 v[64:79], a[104:107], v[176:179], v[64:79]
	ds_read_b128 v[176:179], v192 offset:61440
	v_exp_f32_e32 v212, v60
	v_add_f32_e32 v207, 1.0, v207
	v_add_f32_e32 v208, 1.0, v208
	v_mfma_f32_32x32x16_f16 v[80:95], a[104:107], v[180:183], v[80:95]
	ds_read_b128 v[180:183], v192 offset:62464
	v_exp_f32_e32 v213, v61
	v_add_f32_e32 v209, 1.0, v209
	v_add_f32_e32 v210, 1.0, v210
	s_waitcnt lgkmcnt(2)
	v_mfma_f32_32x32x16_f16 v[64:79], a[108:111], v[184:187], v[64:79]
	ds_read_b128 v[184:187], v192 offset:63488
	v_exp_f32_e32 v214, v62
	v_add_f32_e32 v211, 1.0, v211
	v_add_f32_e32 v212, 1.0, v212
	s_add_u32 s46, s42, 0x0
	s_addc_u32 s47, s43, 0
	global_load_dwordx4 v[0:3], v192, s[46:47] offset:0
	v_mfma_f32_32x32x16_f16 v[80:95], a[108:111], v[188:191], v[80:95]
	ds_read_b128 v[188:191], v192 offset:64512
	global_load_lds_dwordx4 v192, s[44:45] offset:2048 sc1
	v_exp_f32_e32 v215, v63
	v_add_f32_e32 v213, 1.0, v213
	v_add_f32_e32 v214, 1.0, v214
	global_load_dwordx4 v[4:7], v192, s[46:47] offset:1024
	global_load_dwordx4 v[8:11], v192, s[46:47] offset:2048
	s_waitcnt vmcnt(10)
	s_barrier
	v_mfma_f32_32x32x16_f16 v[64:79], a[112:115], v[160:163], v[64:79]
	ds_read_b128 v[160:163], v193 offset:0
	v_add_f32_e32 v215, 1.0, v215
	v_rcp_f32_e32 v200, v200
	global_load_dwordx4 v[12:15], v192, s[46:47] offset:3072
	s_add_u32 s46, s42, 0x1000
	s_addc_u32 s47, s43, 0
	v_mfma_f32_32x32x16_f16 v[80:95], a[112:115], v[164:167], v[80:95]
	ds_read_b128 v[164:167], v193 offset:1024
	v_rcp_f32_e32 v201, v201
	global_load_dwordx4 v[16:19], v192, s[46:47] offset:0
	global_load_dwordx4 v[20:23], v192, s[46:47] offset:1024
	v_mfma_f32_32x32x16_f16 v[64:79], a[116:119], v[168:171], v[64:79]
	ds_read_b128 v[168:171], v193 offset:2048
	v_rcp_f32_e32 v202, v202
	global_load_dwordx4 v[24:27], v192, s[46:47] offset:2048
	global_load_dwordx4 v[28:31], v192, s[46:47] offset:3072
	v_mfma_f32_32x32x16_f16 v[80:95], a[116:119], v[172:175], v[80:95]
	ds_read_b128 v[172:175], v193 offset:3072
	global_load_lds_dwordx4 v192, s[44:45] offset:3072 sc1
	v_rcp_f32_e32 v203, v203
	s_waitcnt lgkmcnt(2)
	v_mfma_f32_32x32x16_f16 v[64:79], a[120:123], v[176:179], v[64:79]
	ds_read_b128 v[176:179], v193 offset:4096
	v_rcp_f32_e32 v204, v204
	v_mfma_f32_32x32x16_f16 v[80:95], a[120:123], v[180:183], v[80:95]
	ds_read_b128 v[180:183], v193 offset:5120
	v_rcp_f32_e32 v205, v205
	v_mul_f32_e32 v204, v204, v140
	v_mfma_f32_32x32x16_f16 v[64:79], a[124:127], v[184:187], v[64:79]
	ds_read_b128 v[184:187], v193 offset:6144
	v_rcp_f32_e32 v206, v206
	v_mul_f32_e32 v205, v205, v141
	v_mfma_f32_32x32x16_f16 v[80:95], a[124:127], v[188:191], v[80:95]
	ds_read_b128 v[188:191], v193 offset:7168
	v_cmp_gt_u32_e32 vcc, 4, v251
	s_cbranch_vccnz .LD_tpoll29
.LD_tok28:
	s_and_b32 s64, s71, 1
	s_lshl_b32 s64, s64, 22
	s_add_u32 s64, s64, s49
	s_add_u32 s64, s64, 0x60000
	s_add_u32 s34, s6, s64
	s_addc_u32 s35, s7, 0
	s_mov_b32 m0, s52
	s_add_u32 s44, s34, 0x0
	s_addc_u32 s45, s35, 0
	global_load_lds_dwordx4 v192, s[44:45] sc1
	v_rcp_f32_e32 v207, v207
	v_mul_f32_e32 v206, v206, v142
	v_mfma_f32_32x32x16_f16 v[64:79], a[128:131], v[160:163], v[64:79]
	ds_read_b128 v[160:163], v193 offset:8192
	v_rcp_f32_e32 v208, v208
	v_mul_f32_e32 v207, v207, v143
	v_mfma_f32_32x32x16_f16 v[80:95], a[128:131], v[164:167], v[80:95]
	ds_read_b128 v[164:167], v193 offset:9216
	v_rcp_f32_e32 v209, v209
	v_fmamk_f32 v208, v208, 0xc0b8aa3b, v198
	s_waitcnt lgkmcnt(2)
	v_mfma_f32_32x32x16_f16 v[64:79], a[132:135], v[168:171], v[64:79]
	ds_read_b128 v[168:171], v193 offset:10240
	v_rcp_f32_e32 v210, v210
	v_fmamk_f32 v209, v209, 0xc0b8aa3b, v198
	v_fma_f32 v140, v200, v208, v204
	v_mfma_f32_32x32x16_f16 v[80:95], a[132:135], v[172:175], v[80:95]
	ds_read_b128 v[172:175], v193 offset:11264
	global_load_lds_dwordx4 v192, s[44:45] offset:1024 sc1
	v_rcp_f32_e32 v211, v211
	v_fmamk_f32 v210, v210, 0xc0b8aa3b, v198
	v_fma_f32 v141, v201, v209, v205
	v_mfma_f32_32x32x16_f16 v[64:79], a[136:139], v[176:179], v[64:79]
	ds_read_b128 v[176:179], v193 offset:12288
	v_rcp_f32_e32 v212, v212
	v_fmamk_f32 v211, v211, 0xc0b8aa3b, v198
	v_fma_f32 v142, v202, v210, v206
	v_mfma_f32_32x32x16_f16 v[80:95], a[136:139], v[180:183], v[80:95]
	ds_read_b128 v[180:183], v193 offset:13312
	v_rcp_f32_e32 v213, v213
	v_fma_f32 v143, v203, v211, v207
	v_mfma_f32_32x32x16_f16 v[64:79], a[140:143], v[184:187], v[64:79]
	ds_read_b128 v[184:187], v193 offset:14336
	v_rcp_f32_e32 v214, v214
	v_mfma_f32_32x32x16_f16 v[80:95], a[140:143], v[188:191], v[80:95]
	ds_read_b128 v[188:191], v193 offset:15360
	global_load_lds_dwordx4 v192, s[44:45] offset:2048 sc1
	v_rcp_f32_e32 v215, v215
	s_waitcnt lgkmcnt(2)
	v_mfma_f32_32x32x16_f16 v[64:79], a[144:147], v[160:163], v[64:79]
	ds_read_b128 v[160:163], v193 offset:16384
	v_exp_f32_e32 v200, v140
	v_mfma_f32_32x32x16_f16 v[80:95], a[144:147], v[164:167], v[80:95]
	ds_read_b128 v[164:167], v193 offset:17408
	v_exp_f32_e32 v201, v141
	v_add_f32_e32 v200, 1.0, v200
	v_mfma_f32_32x32x16_f16 v[64:79], a[148:151], v[168:171], v[64:79]
	ds_read_b128 v[168:171], v193 offset:18432
	v_exp_f32_e32 v202, v142
	v_add_f32_e32 v201, 1.0, v201
	v_mfma_f32_32x32x16_f16 v[80:95], a[148:151], v[172:175], v[80:95]
	ds_read_b128 v[172:175], v193 offset:19456
	global_load_lds_dwordx4 v192, s[44:45] offset:3072 sc1
	v_exp_f32_e32 v203, v143
	v_add_f32_e32 v202, 1.0, v202
	v_mfma_f32_32x32x16_f16 v[64:79], a[152:155], v[176:179], v[64:79]
	ds_read_b128 v[176:179], v193 offset:20480
	v_add_f32_e32 v203, 1.0, v203
	v_rcp_f32_e32 v200, v200
	v_mfma_f32_32x32x16_f16 v[80:95], a[152:155], v[180:183], v[80:95]
	ds_read_b128 v[180:183], v193 offset:21504
	v_rcp_f32_e32 v201, v201
	v_fma_f32 v200, v200, 2.0, -1.0
	s_waitcnt lgkmcnt(2)
	v_mfma_f32_32x32x16_f16 v[64:79], a[156:159], v[184:187], v[64:79]
	ds_read_b128 v[184:187], v193 offset:22528
	v_rcp_f32_e32 v202, v202
	v_fma_f32 v201, v201, 2.0, -1.0
	v_mul_f32_e32 v216, v212, v200
	v_mfma_f32_32x32x16_f16 v[80:95], a[156:159], v[188:191], v[80:95]
	ds_read_b128 v[188:191], v193 offset:23552
	s_mov_b32 m0, s53
	s_add_u32 s44, s34, 0x1000
	s_addc_u32 s45, s35, 0
	global_load_lds_dwordx4 v192, s[44:45] sc1
	v_rcp_f32_e32 v203, v203
	v_fma_f32 v202, v202, 2.0, -1.0
	v_mul_f32_e32 v217, v213, v201
	v_mfma_f32_32x32x16_f16 v[64:79], a[160:163], v[160:163], v[64:79]
	ds_read_b128 v[160:163], v193 offset:24576
	v_fma_f32 v203, v203, 2.0, -1.0
	v_mul_f32_e32 v218, v214, v202
	v_mfma_f32_32x32x16_f16 v[80:95], a[160:163], v[164:167], v[80:95]
	ds_read_b128 v[164:167], v193 offset:25600
	v_mul_f32_e32 v219, v215, v203
	v_mul_f32_e32 v236, v216, v228
	v_mfma_f32_32x32x16_f16 v[64:79], a[164:167], v[168:171], v[64:79]
	ds_read_b128 v[168:171], v193 offset:26624
	v_mul_f32_e32 v237, v216, v232
	v_fmac_f32_e32 v236, v217, v229
	v_mfma_f32_32x32x16_f16 v[80:95], a[164:167], v[172:175], v[80:95]
	ds_read_b128 v[172:175], v193 offset:27648
	global_load_lds_dwordx4 v192, s[44:45] offset:1024 sc1
	v_fmac_f32_e32 v237, v217, v233
	v_fmac_f32_e32 v236, v218, v230
	s_waitcnt lgkmcnt(2)
	v_mfma_f32_32x32x16_f16 v[64:79], a[168:171], v[176:179], v[64:79]
	ds_read_b128 v[176:179], v193 offset:28672
	v_fmac_f32_e32 v237, v218, v234
	v_fmac_f32_e32 v236, v219, v231
	v_mfma_f32_32x32x16_f16 v[80:95], a[168:171], v[180:183], v[80:95]
	ds_read_b128 v[180:183], v193 offset:29696
	v_fmac_f32_e32 v237, v219, v235
	v_mov_b32_e32 v238, v236
	v_mfma_f32_32x32x16_f16 v[64:79], a[172:175], v[184:187], v[64:79]
	ds_read_b128 v[184:187], v193 offset:30720
	v_mov_b32_e32 v240, v237
	v_cvt_pk_f16_f32 v222, v216, v217
	v_mfma_f32_32x32x16_f16 v[80:95], a[172:175], v[188:191], v[80:95]
	ds_read_b128 v[188:191], v193 offset:31744
	global_load_lds_dwordx4 v192, s[44:45] offset:2048 sc1
	v_permlane32_swap_b32_e32 v236, v238
	v_permlane32_swap_b32_e32 v237, v240
	v_add_f32_e32 v238, v236, v238
	v_add_f32_e32 v239, v237, v240
	ds_write_b64 v248, v[238:239] offset:768
	s_waitcnt vmcnt(7)
	s_barrier
	v_mfma_f32_32x32x16_f16 v[64:79], a[176:179], v[160:163], v[64:79]
	ds_read_b128 v[160:163], v193 offset:32768
	v_cvt_pk_f16_f32 v223, v218, v219
	v_mfma_f32_32x32x16_f16 v[80:95], a[176:179], v[164:167], v[80:95]
	ds_read_b128 v[164:167], v193 offset:33792
	v_permlane32_swap_b32_e32 v220, v222
	v_permlane32_swap_b32_e32 v221, v223
	s_cmp_eq_u32 s31, 0
	s_cbranch_scc1 .LD_slow30
	global_store_dwordx4 v195, v[220:223], s[36:37] offset:0

.LD_join33:
	ds_read_b64 v[200:201], v249 offset:512
	ds_read_b64 v[202:203], v249 offset:2560
	ds_read_b64 v[204:205], v249 offset:4608
	ds_read_b64 v[206:207], v249 offset:6656
	v_mfma_f32_32x32x16_f16 v[80:95], a[212:215], v[172:175], v[80:95]
	ds_read_b128 v[172:175], v193 offset:52224
	global_load_lds_dwordx4 v192, s[44:45] offset:3072 sc1
	s_waitcnt lgkmcnt(6)
	v_mfma_f32_32x32x16_f16 v[64:79], a[216:219], v[176:179], v[64:79]
	ds_read_b128 v[176:179], v193 offset:53248
	v_mfma_f32_32x32x16_f16 v[80:95], a[216:219], v[180:183], v[80:95]
	ds_read_b128 v[180:183], v193 offset:54272
	v_mfma_f32_32x32x16_f16 v[64:79], a[220:223], v[184:187], v[64:79]
	ds_read_b128 v[184:187], v193 offset:55296
	v_mfma_f32_32x32x16_f16 v[80:95], a[220:223], v[188:191], v[80:95]
	ds_read_b128 v[188:191], v193 offset:56320
	s_mov_b32 m0, s55
	s_add_u32 s44, s34, 0x9000
	s_addc_u32 s45, s35, 0
	global_load_lds_dwordx4 v192, s[44:45] sc1
	v_mfma_f32_32x32x16_f16 v[64:79], a[224:227], v[160:163], v[64:79]
	ds_read_b128 v[160:163], v193 offset:57344
	v_mfma_f32_32x32x16_f16 v[80:95], a[224:227], v[164:167], v[80:95]
	ds_read_b128 v[164:167], v193 offset:58368
	s_waitcnt lgkmcnt(2)
	v_mfma_f32_32x32x16_f16 v[64:79], a[228:231], v[168:171], v[64:79]
	ds_read_b128 v[168:171], v193 offset:59392
	v_mfma_f32_32x32x16_f16 v[80:95], a[228:231], v[172:175], v[80:95]
	ds_read_b128 v[172:175], v193 offset:60416
	global_load_lds_dwordx4 v192, s[44:45] offset:1024 sc1
	v_mfma_f32_32x32x16_f16 v[64:79], a[232:235], v[176:179], v[64:79]
	ds_read_b128 v[176:179], v193 offset:61440
	v_mfma_f32_32x32x16_f16 v[80:95], a[232:235], v[180:183], v[80:95]
	ds_read_b128 v[180:183], v193 offset:62464
	v_mfma_f32_32x32x16_f16 v[64:79], a[236:239], v[184:187], v[64:79]
	ds_read_b128 v[184:187], v193 offset:63488
	v_add_f32_e32 v200, v200, v202
	v_add_f32_e32 v201, v201, v203
	v_add_f32_e32 v200, v200, v204
	v_add_f32_e32 v201, v201, v205
	v_add_f32_e32 v200, v200, v206
	v_add_f32_e32 v201, v201, v207
	global_store_dwordx2 v250, v[200:201], s[72:73]
	v_mfma_f32_32x32x16_f16 v[80:95], a[236:239], v[188:191], v[80:95]
	ds_read_b128 v[188:191], v193 offset:64512
	global_load_lds_dwordx4 v192, s[44:45] offset:2048 sc1
	s_waitcnt vmcnt(9)
	s_barrier
	s_waitcnt lgkmcnt(2)
	v_mfma_f32_32x32x16_f16 v[64:79], a[240:243], v[160:163], v[64:79]
	ds_read_b128 v[160:163], v192 offset:0
	v_mfma_f32_32x32x16_f16 v[80:95], a[240:243], v[164:167], v[80:95]
	ds_read_b128 v[164:167], v192 offset:1024
	v_mfma_f32_32x32x16_f16 v[64:79], a[244:247], v[168:171], v[64:79]
	ds_read_b128 v[168:171], v192 offset:2048
	s_and_b32 s64, s33, 1
	s_lshl_b32 s64, s64, 22
	s_add_u32 s64, s64, s50
	s_add_u32 s64, s64, 0x40000
	s_add_u32 s36, s6, s64
	s_addc_u32 s37, s7, 0
	s_lshl_b32 s64, s33, 3
	s_add_u32 s64, s64, s29
	s_lshl_b32 s64, s64, 5
	s_add_u32 s64, s64, s30
	s_lshl_b32 s64, s64, 2
	s_add_u32 s40, s8, s64
	s_addc_u32 s41, s9, 0
	s_lshl_b32 s64, s33, 19
	s_add_u32 s64, s64, 0x400
	s_add_u32 s72, s62, s64
	s_addc_u32 s73, s63, 0
	v_mfma_f32_32x32x16_f16 v[80:95], a[244:247], v[172:175], v[80:95]
	ds_read_b128 v[172:175], v192 offset:3072
	global_load_lds_dwordx4 v192, s[44:45] offset:3072 sc1
	v_mfma_f32_32x32x16_f16 v[64:79], a[248:251], v[176:179], v[64:79]
	ds_read_b128 v[176:179], v192 offset:4096
	v_mfma_f32_32x32x16_f16 v[80:95], a[248:251], v[180:183], v[80:95]
	ds_read_b128 v[180:183], v192 offset:5120
	s_waitcnt lgkmcnt(2)
	v_mfma_f32_32x32x16_f16 v[64:79], a[252:255], v[184:187], v[64:79]
	ds_read_b128 v[184:187], v192 offset:6144
	v_mfma_f32_32x32x16_f16 v[80:95], a[252:255], v[188:191], v[80:95]
	ds_read_b128 v[188:191], v192 offset:7168
	s_mov_b32 m0, s56
	s_add_u32 s44, s34, 0x10000
	s_addc_u32 s45, s35, 0
	global_load_lds_dwordx4 v192, s[44:45] sc1
	s_nop 3
	s_waitcnt lgkmcnt(2)
	v_mfma_f32_32x32x16_f16 v[96:111], a[0:3], v[160:163], v[96:111]
	ds_read_b128 v[160:163], v192 offset:8192
	v_exp_f32_e32 v200, v64
	v_mfma_f32_32x32x16_f16 v[112:127], a[0:3], v[164:167], v[112:127]
	ds_read_b128 v[164:167], v192 offset:9216
	s_lshl_b32 s64, s33, 3
	s_add_u32 s64, s64, s29
	s_lshl_b32 s64, s64, 7
	s_add_u32 s38, s8, s64
	s_addc_u32 s39, s9, 0
	global_load_dword v251, v196, s[38:39] sc1
	v_exp_f32_e32 v201, v65
	v_add_f32_e32 v200, 1.0, v200
	v_mfma_f32_32x32x16_f16 v[96:111], a[4:7], v[168:171], v[96:111]
	ds_read_b128 v[168:171], v192 offset:10240
	v_exp_f32_e32 v202, v66
	v_add_f32_e32 v201, 1.0, v201
	v_mfma_f32_32x32x16_f16 v[112:127], a[4:7], v[172:175], v[112:127]
	ds_read_b128 v[172:175], v192 offset:11264
	global_load_lds_dwordx4 v192, s[44:45] offset:1024 sc1
	v_exp_f32_e32 v203, v67
	v_add_f32_e32 v202, 1.0, v202
	v_mfma_f32_32x32x16_f16 v[96:111], a[8:11], v[176:179], v[96:111]
	ds_read_b128 v[176:179], v192 offset:12288
	v_exp_f32_e32 v204, v68
	v_add_f32_e32 v203, 1.0, v203
	v_mfma_f32_32x32x16_f16 v[112:127], a[8:11], v[180:183], v[112:127]
	ds_read_b128 v[180:183], v192 offset:13312
	v_exp_f32_e32 v205, v69
	v_add_f32_e32 v204, 1.0, v204
	s_waitcnt lgkmcnt(2)
	v_mfma_f32_32x32x16_f16 v[96:111], a[12:15], v[184:187], v[96:111]
	ds_read_b128 v[184:187], v192 offset:14336
	v_exp_f32_e32 v206, v70
	v_add_f32_e32 v205, 1.0, v205
	v_mfma_f32_32x32x16_f16 v[112:127], a[12:15], v[188:191], v[112:127]
	ds_read_b128 v[188:191], v192 offset:15360
	global_load_lds_dwordx4 v192, s[44:45] offset:2048 sc1
	v_exp_f32_e32 v207, v71
	v_add_f32_e32 v206, 1.0, v206
	v_mfma_f32_32x32x16_f16 v[96:111], a[16:19], v[160:163], v[96:111]
	ds_read_b128 v[160:163], v192 offset:16384
	v_exp_f32_e32 v208, v72
	v_add_f32_e32 v207, 1.0, v207
	v_mfma_f32_32x32x16_f16 v[112:127], a[16:19], v[164:167], v[112:127]
	ds_read_b128 v[164:167], v192 offset:17408
	v_exp_f32_e32 v209, v73
	v_add_f32_e32 v208, 1.0, v208
	v_mfma_f32_32x32x16_f16 v[96:111], a[20:23], v[168:171], v[96:111]
	ds_read_b128 v[168:171], v192 offset:18432
	v_exp_f32_e32 v210, v74
	v_add_f32_e32 v209, 1.0, v209
	v_mfma_f32_32x32x16_f16 v[112:127], a[20:23], v[172:175], v[112:127]
	ds_read_b128 v[172:175], v192 offset:19456
	global_load_lds_dwordx4 v192, s[44:45] offset:3072 sc1
	v_exp_f32_e32 v211, v75
	v_add_f32_e32 v210, 1.0, v210
	s_waitcnt lgkmcnt(2)
	v_mfma_f32_32x32x16_f16 v[96:111], a[24:27], v[176:179], v[96:111]
	ds_read_b128 v[176:179], v192 offset:20480
	v_exp_f32_e32 v212, v76
	v_add_f32_e32 v211, 1.0, v211
	v_mfma_f32_32x32x16_f16 v[112:127], a[24:27], v[180:183], v[112:127]
	ds_read_b128 v[180:183], v192 offset:21504
	v_exp_f32_e32 v213, v77
	v_add_f32_e32 v212, 1.0, v212
	v_mfma_f32_32x32x16_f16 v[96:111], a[28:31], v[184:187], v[96:111]
	ds_read_b128 v[184:187], v192 offset:22528
	v_exp_f32_e32 v214, v78
	v_add_f32_e32 v213, 1.0, v213
	v_mfma_f32_32x32x16_f16 v[112:127], a[28:31], v[188:191], v[112:127]
	ds_read_b128 v[188:191], v192 offset:23552
	s_mov_b32 m0, s57
	s_add_u32 s44, s34, 0x11000
	s_addc_u32 s45, s35, 0
	global_load_lds_dwordx4 v192, s[44:45] sc1
	v_exp_f32_e32 v215, v79
	v_add_f32_e32 v214, 1.0, v214
	v_mfma_f32_32x32x16_f16 v[96:111], a[32:35], v[160:163], v[96:111]
	ds_read_b128 v[160:163], v192 offset:24576
	v_add_f32_e32 v215, 1.0, v215
	v_rcp_f32_e32 v200, v200
	v_mfma_f32_32x32x16_f16 v[112:127], a[32:35], v[164:167], v[112:127]
	ds_read_b128 v[164:167], v192 offset:25600
	v_rcp_f32_e32 v201, v201
	s_waitcnt lgkmcnt(2)
	v_mfma_f32_32x32x16_f16 v[96:111], a[36:39], v[168:171], v[96:111]
	ds_read_b128 v[168:171], v192 offset:26624
	v_rcp_f32_e32 v202, v202
	v_mfma_f32_32x32x16_f16 v[112:127], a[36:39], v[172:175], v[112:127]
	ds_read_b128 v[172:175], v192 offset:27648
	global_load_lds_dwordx4 v192, s[44:45] offset:1024 sc1
	v_rcp_f32_e32 v203, v203
	v_mfma_f32_32x32x16_f16 v[96:111], a[40:43], v[176:179], v[96:111]
	ds_read_b128 v[176:179], v192 offset:28672
	v_rcp_f32_e32 v204, v204
	v_mfma_f32_32x32x16_f16 v[112:127], a[40:43], v[180:183], v[112:127]
	ds_read_b128 v[180:183], v192 offset:29696
	v_rcp_f32_e32 v205, v205
	v_mul_f32_e32 v204, v204, v144
	v_mfma_f32_32x32x16_f16 v[96:111], a[44:47], v[184:187], v[96:111]
	ds_read_b128 v[184:187], v192 offset:30720
	v_rcp_f32_e32 v206, v206
	v_mul_f32_e32 v205, v205, v145
	v_mfma_f32_32x32x16_f16 v[112:127], a[44:47], v[188:191], v[112:127]
	ds_read_b128 v[188:191], v192 offset:31744
	global_load_lds_dwordx4 v192, s[44:45] offset:2048 sc1
	v_rcp_f32_e32 v207, v207
	v_mul_f32_e32 v206, v206, v146
	s_waitcnt vmcnt(8)
	s_barrier
	s_waitcnt lgkmcnt(2)
	v_mfma_f32_32x32x16_f16 v[96:111], a[48:51], v[160:163], v[96:111]
	ds_read_b128 v[160:163], v192 offset:32768
	v_rcp_f32_e32 v208, v208
	v_mul_f32_e32 v207, v207, v147
	v_mfma_f32_32x32x16_f16 v[112:127], a[48:51], v[164:167], v[112:127]
	ds_read_b128 v[164:167], v192 offset:33792
	v_rcp_f32_e32 v209, v209
	v_fmamk_f32 v208, v208, 0xc0b8aa3b, v198
	v_mfma_f32_32x32x16_f16 v[96:111], a[52:55], v[168:171], v[96:111]
	ds_read_b128 v[168:171], v192 offset:34816
	v_rcp_f32_e32 v210, v210
	v_fmamk_f32 v209, v209, 0xc0b8aa3b, v198
	v_fma_f32 v144, v200, v208, v204
	v_mfma_f32_32x32x16_f16 v[112:127], a[52:55], v[172:175], v[112:127]
	ds_read_b128 v[172:175], v192 offset:35840
	global_load_lds_dwordx4 v192, s[44:45] offset:3072 sc1
	v_rcp_f32_e32 v211, v211
	v_fmamk_f32 v210, v210, 0xc0b8aa3b, v198
	v_fma_f32 v145, v201, v209, v205
	v_mfma_f32_32x32x16_f16 v[96:111], a[56:59], v[176:179], v[96:111]
	ds_read_b128 v[176:179], v192 offset:36864
	v_rcp_f32_e32 v212, v212
	v_fmamk_f32 v211, v211, 0xc0b8aa3b, v198
	v_fma_f32 v146, v202, v210, v206
	v_mfma_f32_32x32x16_f16 v[112:127], a[56:59], v[180:183], v[112:127]
	ds_read_b128 v[180:183], v192 offset:37888
	v_rcp_f32_e32 v213, v213
	v_fma_f32 v147, v203, v211, v207
	s_waitcnt lgkmcnt(2)
	v_mfma_f32_32x32x16_f16 v[96:111], a[60:63], v[184:187], v[96:111]
	ds_read_b128 v[184:187], v192 offset:38912
	v_rcp_f32_e32 v214, v214
	v_mfma_f32_32x32x16_f16 v[112:127], a[60:63], v[188:191], v[112:127]
	ds_read_b128 v[188:191], v192 offset:39936
	s_mov_b32 m0, s58
	s_add_u32 s44, s34, 0x18000
	s_addc_u32 s45, s35, 0
	global_load_lds_dwordx4 v192, s[44:45] sc1
	v_rcp_f32_e32 v215, v215
	v_mfma_f32_32x32x16_f16 v[96:111], a[64:67], v[160:163], v[96:111]
	ds_read_b128 v[160:163], v192 offset:40960
	v_exp_f32_e32 v200, v144
	v_mfma_f32_32x32x16_f16 v[112:127], a[64:67], v[164:167], v[112:127]
	ds_read_b128 v[164:167], v192 offset:41984
	v_exp_f32_e32 v201, v145
	v_add_f32_e32 v200, 1.0, v200
	v_mfma_f32_32x32x16_f16 v[96:111], a[68:71], v[168:171], v[96:111]
	ds_read_b128 v[168:171], v192 offset:43008
	v_exp_f32_e32 v202, v146
	v_add_f32_e32 v201, 1.0, v201
	v_mfma_f32_32x32x16_f16 v[112:127], a[68:71], v[172:175], v[112:127]
	ds_read_b128 v[172:175], v192 offset:44032
	global_load_lds_dwordx4 v192, s[44:45] offset:1024 sc1
	v_exp_f32_e32 v203, v147
	v_add_f32_e32 v202, 1.0, v202
	s_waitcnt lgkmcnt(2)
	v_mfma_f32_32x32x16_f16 v[96:111], a[72:75], v[176:179], v[96:111]
	ds_read_b128 v[176:179], v192 offset:45056
	v_add_f32_e32 v203, 1.0, v203
	v_rcp_f32_e32 v200, v200
	v_mfma_f32_32x32x16_f16 v[112:127], a[72:75], v[180:183], v[112:127]
	ds_read_b128 v[180:183], v192 offset:46080
	v_rcp_f32_e32 v201, v201
	v_fma_f32 v200, v200, 2.0, -1.0
	v_mfma_f32_32x32x16_f16 v[96:111], a[76:79], v[184:187], v[96:111]
	ds_read_b128 v[184:187], v192 offset:47104
	v_rcp_f32_e32 v202, v202
	v_fma_f32 v201, v201, 2.0, -1.0
	v_mul_f32_e32 v216, v212, v200
	v_mfma_f32_32x32x16_f16 v[112:127], a[76:79], v[188:191], v[112:127]
	ds_read_b128 v[188:191], v192 offset:48128
	global_load_lds_dwordx4 v192, s[44:45] offset:2048 sc1
	v_rcp_f32_e32 v203, v203
	v_fma_f32 v202, v202, 2.0, -1.0
	v_mul_f32_e32 v217, v213, v201
	v_mfma_f32_32x32x16_f16 v[96:111], a[80:83], v[160:163], v[96:111]
	ds_read_b128 v[160:163], v192 offset:49152
	v_fma_f32 v203, v203, 2.0, -1.0
	v_mul_f32_e32 v218, v214, v202
	v_exp_f32_e32 v200, v80
	v_mfma_f32_32x32x16_f16 v[112:127], a[80:83], v[164:167], v[112:127]
	ds_read_b128 v[164:167], v192 offset:50176
	v_mul_f32_e32 v219, v215, v203
	v_mul_f32_e32 v236, v216, v228
	v_exp_f32_e32 v201, v81
	s_waitcnt lgkmcnt(2)
	v_mfma_f32_32x32x16_f16 v[96:111], a[84:87], v[168:171], v[96:111]
	ds_read_b128 v[168:171], v192 offset:51200
	v_mul_f32_e32 v237, v216, v232
	v_fmac_f32_e32 v236, v217, v229
	v_exp_f32_e32 v202, v82
	v_mfma_f32_32x32x16_f16 v[112:127], a[84:87], v[172:175], v[112:127]
	ds_read_b128 v[172:175], v192 offset:52224
	global_load_lds_dwordx4 v192, s[44:45] offset:3072 sc1
	v_fmac_f32_e32 v237, v217, v233
	v_fmac_f32_e32 v236, v218, v230
	v_exp_f32_e32 v203, v83
	v_mfma_f32_32x32x16_f16 v[96:111], a[88:91], v[176:179], v[96:111]
	ds_read_b128 v[176:179], v192 offset:53248
	v_fmac_f32_e32 v237, v218, v234
	v_fmac_f32_e32 v236, v219, v231
	v_exp_f32_e32 v204, v84
	v_mfma_f32_32x32x16_f16 v[112:127], a[88:91], v[180:183], v[112:127]
	ds_read_b128 v[180:183], v192 offset:54272
	v_fmac_f32_e32 v237, v219, v235
	v_mov_b32_e32 v238, v236
	v_exp_f32_e32 v205, v85
	v_mfma_f32_32x32x16_f16 v[96:111], a[92:95], v[184:187], v[96:111]
	ds_read_b128 v[184:187], v192 offset:55296
	v_mov_b32_e32 v240, v237
	v_cvt_pk_f16_f32 v220, v216, v217
	v_exp_f32_e32 v206, v86
	v_mfma_f32_32x32x16_f16 v[112:127], a[92:95], v[188:191], v[112:127]
	ds_read_b128 v[188:191], v192 offset:56320
	s_mov_b32 m0, s59
	s_add_u32 s44, s34, 0x19000
	s_addc_u32 s45, s35, 0
	global_load_lds_dwordx4 v192, s[44:45] sc1
	v_permlane32_swap_b32_e32 v236, v238
	v_permlane32_swap_b32_e32 v237, v240
	v_add_f32_e32 v238, v236, v238
	v_add_f32_e32 v239, v237, v240
	ds_write_b64 v248, v[238:239] offset:1024
	v_exp_f32_e32 v207, v87
	s_waitcnt lgkmcnt(3)
	v_mfma_f32_32x32x16_f16 v[96:111], a[96:99], v[160:163], v[96:111]
	ds_read_b128 v[160:163], v192 offset:57344
	v_cvt_pk_f16_f32 v221, v218, v219
	v_exp_f32_e32 v208, v88
	v_add_f32_e32 v200, 1.0, v200
	v_mfma_f32_32x32x16_f16 v[112:127], a[96:99], v[164:167], v[112:127]
	ds_read_b128 v[164:167], v192 offset:58368
	v_exp_f32_e32 v209, v89
	v_add_f32_e32 v201, 1.0, v201
	v_add_f32_e32 v202, 1.0, v202
	v_mfma_f32_32x32x16_f16 v[96:111], a[100:103], v[168:171], v[96:111]
	ds_read_b128 v[168:171], v192 offset:59392
	v_exp_f32_e32 v210, v90
	v_add_f32_e32 v203, 1.0, v203
	v_add_f32_e32 v204, 1.0, v204
	v_mfma_f32_32x32x16_f16 v[112:127], a[100:103], v[172:175], v[112:127]
	ds_read_b128 v[172:175], v192 offset:60416
	global_load_lds_dwordx4 v192, s[44:45] offset:1024 sc1
	v_exp_f32_e32 v211, v91
	v_add_f32_e32 v205, 1.0, v205
	v_add_f32_e32 v206, 1.0, v206
	v_mfma_f32_32x32x16_f16 v[96:111], a[104:107], v[176:179], v[96:111]
	ds_read_b128 v[176:179], v192 offset:61440
	v_exp_f32_e32 v212, v92
	v_add_f32_e32 v207, 1.0, v207
	v_add_f32_e32 v208, 1.0, v208
	v_mfma_f32_32x32x16_f16 v[112:127], a[104:107], v[180:183], v[112:127]
	ds_read_b128 v[180:183], v192 offset:62464
	v_exp_f32_e32 v213, v93
	v_add_f32_e32 v209, 1.0, v209
	v_add_f32_e32 v210, 1.0, v210
	s_waitcnt lgkmcnt(2)
	v_mfma_f32_32x32x16_f16 v[96:111], a[108:111], v[184:187], v[96:111]
	ds_read_b128 v[184:187], v192 offset:63488
	v_exp_f32_e32 v214, v94
	v_add_f32_e32 v211, 1.0, v211
	v_add_f32_e32 v212, 1.0, v212
	s_add_u32 s46, s42, 0x2000
	s_addc_u32 s47, s43, 0
	global_load_dwordx4 v[32:35], v192, s[46:47] offset:0
	v_mfma_f32_32x32x16_f16 v[112:127], a[108:111], v[188:191], v[112:127]
	ds_read_b128 v[188:191], v192 offset:64512
	global_load_lds_dwordx4 v192, s[44:45] offset:2048 sc1
	v_exp_f32_e32 v215, v95
	v_add_f32_e32 v213, 1.0, v213
	v_add_f32_e32 v214, 1.0, v214
	global_load_dwordx4 v[36:39], v192, s[46:47] offset:1024
	global_load_dwordx4 v[40:43], v192, s[46:47] offset:2048
	s_waitcnt vmcnt(10)
	s_barrier
	v_mfma_f32_32x32x16_f16 v[96:111], a[112:115], v[160:163], v[96:111]
	ds_read_b128 v[160:163], v193 offset:0
	v_add_f32_e32 v215, 1.0, v215
	v_rcp_f32_e32 v200, v200
	global_load_dwordx4 v[44:47], v192, s[46:47] offset:3072
	s_add_u32 s46, s42, 0x3000
	s_addc_u32 s47, s43, 0
	v_mfma_f32_32x32x16_f16 v[112:127], a[112:115], v[164:167], v[112:127]
	ds_read_b128 v[164:167], v193 offset:1024
	v_rcp_f32_e32 v201, v201
	global_load_dwordx4 v[48:51], v192, s[46:47] offset:0
	global_load_dwordx4 v[52:55], v192, s[46:47] offset:1024
	v_mfma_f32_32x32x16_f16 v[96:111], a[116:119], v[168:171], v[96:111]
	ds_read_b128 v[168:171], v193 offset:2048
	v_rcp_f32_e32 v202, v202
	global_load_dwordx4 v[56:59], v192, s[46:47] offset:2048
	global_load_dwordx4 v[60:63], v192, s[46:47] offset:3072
	v_mfma_f32_32x32x16_f16 v[112:127], a[116:119], v[172:175], v[112:127]
	ds_read_b128 v[172:175], v193 offset:3072
	global_load_lds_dwordx4 v192, s[44:45] offset:3072 sc1
	v_rcp_f32_e32 v203, v203
	s_waitcnt lgkmcnt(2)
	v_mfma_f32_32x32x16_f16 v[96:111], a[120:123], v[176:179], v[96:111]
	ds_read_b128 v[176:179], v193 offset:4096
	v_rcp_f32_e32 v204, v204
	v_mfma_f32_32x32x16_f16 v[112:127], a[120:123], v[180:183], v[112:127]
	ds_read_b128 v[180:183], v193 offset:5120
	v_rcp_f32_e32 v205, v205
	v_mul_f32_e32 v204, v204, v148
	v_mfma_f32_32x32x16_f16 v[96:111], a[124:127], v[184:187], v[96:111]
	ds_read_b128 v[184:187], v193 offset:6144
	v_rcp_f32_e32 v206, v206
	v_mul_f32_e32 v205, v205, v149
	v_mfma_f32_32x32x16_f16 v[112:127], a[124:127], v[188:191], v[112:127]
	ds_read_b128 v[188:191], v193 offset:7168
	v_cmp_gt_u32_e32 vcc, 1, v251
	s_cbranch_vccnz .LD_tpoll35
.LD_tok34:
	s_and_b32 s64, s33, 1
	s_lshl_b32 s64, s64, 22
	s_add_u32 s64, s64, s49
	s_add_u32 s34, s6, s64
	s_addc_u32 s35, s7, 0
	s_mov_b32 m0, s52
	s_add_u32 s44, s34, 0x0
	s_addc_u32 s45, s35, 0
	global_load_lds_dwordx4 v192, s[44:45] sc1
	v_rcp_f32_e32 v207, v207
	v_mul_f32_e32 v206, v206, v150
	v_mfma_f32_32x32x16_f16 v[96:111], a[128:131], v[160:163], v[96:111]
	ds_read_b128 v[160:163], v193 offset:8192
	v_rcp_f32_e32 v208, v208
	v_mul_f32_e32 v207, v207, v151
	v_mfma_f32_32x32x16_f16 v[112:127], a[128:131], v[164:167], v[112:127]
	ds_read_b128 v[164:167], v193 offset:9216
	v_rcp_f32_e32 v209, v209
	v_fmamk_f32 v208, v208, 0xc0b8aa3b, v198
	s_waitcnt lgkmcnt(2)
	v_mfma_f32_32x32x16_f16 v[96:111], a[132:135], v[168:171], v[96:111]
	ds_read_b128 v[168:171], v193 offset:10240
	v_rcp_f32_e32 v210, v210
	v_fmamk_f32 v209, v209, 0xc0b8aa3b, v198
	v_fma_f32 v148, v200, v208, v204
	v_mfma_f32_32x32x16_f16 v[112:127], a[132:135], v[172:175], v[112:127]
	ds_read_b128 v[172:175], v193 offset:11264
	global_load_lds_dwordx4 v192, s[44:45] offset:1024 sc1
	v_rcp_f32_e32 v211, v211
	v_fmamk_f32 v210, v210, 0xc0b8aa3b, v198
	v_fma_f32 v149, v201, v209, v205
	v_mfma_f32_32x32x16_f16 v[96:111], a[136:139], v[176:179], v[96:111]
	ds_read_b128 v[176:179], v193 offset:12288
	v_rcp_f32_e32 v212, v212
	v_fmamk_f32 v211, v211, 0xc0b8aa3b, v198
	v_fma_f32 v150, v202, v210, v206
	v_mfma_f32_32x32x16_f16 v[112:127], a[136:139], v[180:183], v[112:127]
	ds_read_b128 v[180:183], v193 offset:13312
	v_rcp_f32_e32 v213, v213
	v_fma_f32 v151, v203, v211, v207
	v_mfma_f32_32x32x16_f16 v[96:111], a[140:143], v[184:187], v[96:111]
	ds_read_b128 v[184:187], v193 offset:14336
	v_rcp_f32_e32 v214, v214
	v_mfma_f32_32x32x16_f16 v[112:127], a[140:143], v[188:191], v[112:127]
	ds_read_b128 v[188:191], v193 offset:15360
	global_load_lds_dwordx4 v192, s[44:45] offset:2048 sc1
	v_rcp_f32_e32 v215, v215
	s_waitcnt lgkmcnt(2)
	v_mfma_f32_32x32x16_f16 v[96:111], a[144:147], v[160:163], v[96:111]
	ds_read_b128 v[160:163], v193 offset:16384
	v_exp_f32_e32 v200, v148
	v_mfma_f32_32x32x16_f16 v[112:127], a[144:147], v[164:167], v[112:127]
	ds_read_b128 v[164:167], v193 offset:17408
	v_exp_f32_e32 v201, v149
	v_add_f32_e32 v200, 1.0, v200
	v_mfma_f32_32x32x16_f16 v[96:111], a[148:151], v[168:171], v[96:111]
	ds_read_b128 v[168:171], v193 offset:18432
	v_exp_f32_e32 v202, v150
	v_add_f32_e32 v201, 1.0, v201
	v_mfma_f32_32x32x16_f16 v[112:127], a[148:151], v[172:175], v[112:127]
	ds_read_b128 v[172:175], v193 offset:19456
	global_load_lds_dwordx4 v192, s[44:45] offset:3072 sc1
	v_exp_f32_e32 v203, v151
	v_add_f32_e32 v202, 1.0, v202
	v_mfma_f32_32x32x16_f16 v[96:111], a[152:155], v[176:179], v[96:111]
	ds_read_b128 v[176:179], v193 offset:20480
	v_add_f32_e32 v203, 1.0, v203
	v_rcp_f32_e32 v200, v200
	v_mfma_f32_32x32x16_f16 v[112:127], a[152:155], v[180:183], v[112:127]
	ds_read_b128 v[180:183], v193 offset:21504
	v_rcp_f32_e32 v201, v201
	v_fma_f32 v200, v200, 2.0, -1.0
	s_waitcnt lgkmcnt(2)
	v_mfma_f32_32x32x16_f16 v[96:111], a[156:159], v[184:187], v[96:111]
	ds_read_b128 v[184:187], v193 offset:22528
	v_rcp_f32_e32 v202, v202
	v_fma_f32 v201, v201, 2.0, -1.0
	v_mul_f32_e32 v216, v212, v200
	v_mfma_f32_32x32x16_f16 v[112:127], a[156:159], v[188:191], v[112:127]
	ds_read_b128 v[188:191], v193 offset:23552
	s_mov_b32 m0, s53
	s_add_u32 s44, s34, 0x1000
	s_addc_u32 s45, s35, 0
	global_load_lds_dwordx4 v192, s[44:45] sc1
	v_rcp_f32_e32 v203, v203
	v_fma_f32 v202, v202, 2.0, -1.0
	v_mul_f32_e32 v217, v213, v201
	v_mfma_f32_32x32x16_f16 v[96:111], a[160:163], v[160:163], v[96:111]
	ds_read_b128 v[160:163], v193 offset:24576
	v_fma_f32 v203, v203, 2.0, -1.0
	v_mul_f32_e32 v218, v214, v202
	v_mfma_f32_32x32x16_f16 v[112:127], a[160:163], v[164:167], v[112:127]
	ds_read_b128 v[164:167], v193 offset:25600
	v_mul_f32_e32 v219, v215, v203
	v_mul_f32_e32 v236, v216, v228
	v_mfma_f32_32x32x16_f16 v[96:111], a[164:167], v[168:171], v[96:111]
	ds_read_b128 v[168:171], v193 offset:26624
	v_mul_f32_e32 v237, v216, v232
	v_fmac_f32_e32 v236, v217, v229
	v_mfma_f32_32x32x16_f16 v[112:127], a[164:167], v[172:175], v[112:127]
	ds_read_b128 v[172:175], v193 offset:27648
	global_load_lds_dwordx4 v192, s[44:45] offset:1024 sc1
	v_fmac_f32_e32 v237, v217, v233
	v_fmac_f32_e32 v236, v218, v230
	s_waitcnt lgkmcnt(2)
	v_mfma_f32_32x32x16_f16 v[96:111], a[168:171], v[176:179], v[96:111]
	ds_read_b128 v[176:179], v193 offset:28672
	v_fmac_f32_e32 v237, v218, v234
	v_fmac_f32_e32 v236, v219, v231
	v_mfma_f32_32x32x16_f16 v[112:127], a[168:171], v[180:183], v[112:127]
	ds_read_b128 v[180:183], v193 offset:29696
	v_fmac_f32_e32 v237, v219, v235
	v_mov_b32_e32 v238, v236
	v_mfma_f32_32x32x16_f16 v[96:111], a[172:175], v[184:187], v[96:111]
	ds_read_b128 v[184:187], v193 offset:30720
	v_mov_b32_e32 v240, v237
	v_cvt_pk_f16_f32 v222, v216, v217
	v_mfma_f32_32x32x16_f16 v[112:127], a[172:175], v[188:191], v[112:127]
	ds_read_b128 v[188:191], v193 offset:31744
	global_load_lds_dwordx4 v192, s[44:45] offset:2048 sc1
	v_permlane32_swap_b32_e32 v236, v238
	v_permlane32_swap_b32_e32 v237, v240
	v_add_f32_e32 v238, v236, v238
	v_add_f32_e32 v239, v237, v240
	ds_write_b64 v248, v[238:239] offset:1280
	s_waitcnt vmcnt(7)
	s_barrier
	v_mfma_f32_32x32x16_f16 v[96:111], a[176:179], v[160:163], v[96:111]
	ds_read_b128 v[160:163], v193 offset:32768
	v_cvt_pk_f16_f32 v223, v218, v219
	v_mfma_f32_32x32x16_f16 v[112:127], a[176:179], v[164:167], v[112:127]
	ds_read_b128 v[164:167], v193 offset:33792
	v_permlane32_swap_b32_e32 v220, v222
	v_permlane32_swap_b32_e32 v221, v223
	s_cmp_eq_u32 s31, 0
	s_cbranch_scc1 .LD_slow36
	global_store_dwordx4 v195, v[220:223], s[36:37] offset:0
